# baseline (speedup 1.0000x reference)
_Z15k3_pairs_slicedPKDv4_jPKfPKiS5_PiPf:
	s_and_b32 s20, s2, 7
	s_load_dwordx8 s[4:11], s[0:1], 0x0
	s_lshl_b32 s3, s2, 7
	v_lshlrev_b32_e32 v2, 2, v0
	s_and_b32 s3, s3, 0x7ffffc00
	v_and_b32_e32 v2, 0x300, v2
	v_and_b32_e32 v1, 63, v0
	v_or_b32_e32 v54, s3, v2
	v_or_b32_e32 v40, v54, v1
	v_mov_b32_e32 v41, 0
	v_lshlrev_b64 v[4:5], 2, v[40:41]
	s_waitcnt lgkmcnt(0)
	v_lshl_add_u64 v[2:3], s[8:9], 0, v[4:5]
	global_load_dword v52, v[2:3], off
	v_lshl_add_u64 v[4:5], s[10:11], 0, v[4:5]
	global_load_dword v53, v[4:5], off
	v_bfe_u32 v55, v0, 3, 3
	v_lshlrev_b32_e32 v44, 2, v55
	s_and_b32 s8, s2, 7
	v_and_b32_e32 v51, 7, v0
	s_lshl_b32 s2, s8, 9
	global_load_dword v50, v[2:3], off offset:256
	global_load_dword v48, v[2:3], off offset:512
	global_load_dword v45, v[2:3], off offset:768
	global_load_dword v49, v[4:5], off offset:256
	global_load_dword v47, v[4:5], off offset:512
	global_load_dword v46, v[4:5], off offset:768
	s_add_u32 s2, s6, s2
	s_mul_i32 s8, s8, 0xc35000
	s_addc_u32 s3, s7, 0
	s_add_u32 s4, s4, s8
	v_lshlrev_b32_e32 v40, 4, v51
	s_addc_u32 s5, s5, 0
	v_lshl_add_u64 v[42:43], s[4:5], 0, v[40:41]
	v_lshlrev_b32_e32 v40, 6, v51
	v_lshlrev_b32_e32 v56, 3, v51
	v_mov_b32_e32 v63, v41
	v_mov_b32_e32 v72, v41
	v_mov_b32_e32 v73, v41
	v_cmp_eq_u32_e32 vcc, 0, v51
	s_load_dwordx4 s[16:19], s[0:1], 0x20
	v_cmp_eq_u32_e64 s[0:1], 1, v51
	v_cmp_eq_u32_e64 s[4:5], 3, v51
	v_cmp_eq_u32_e64 s[6:7], 4, v51
	v_cmp_eq_u32_e64 s[8:9], 5, v51
	v_cmp_eq_u32_e64 s[10:11], 6, v51
	v_cmp_eq_u32_e64 s[12:13], 7, v51
	s_waitcnt vmcnt(7)
	ds_bpermute_b32 v0, v44, v52
	ds_bpermute_b32 v58, v44, v52 offset:128
	s_waitcnt vmcnt(6)
	ds_bpermute_b32 v2, v44, v53
	ds_bpermute_b32 v60, v44, v53 offset:128
	ds_bpermute_b32 v62, v44, v52 offset:160
	s_waitcnt lgkmcnt(0)
	v_ashrrev_i32_e32 v1, 31, v0
	v_lshlrev_b64 v[0:1], 7, v[0:1]
	v_ashrrev_i32_e32 v3, 31, v2
	v_lshlrev_b64 v[2:3], 7, v[2:3]
	v_lshl_add_u64 v[0:1], v[42:43], 0, v[0:1]
	v_lshl_add_u64 v[2:3], v[42:43], 0, v[2:3]
	global_load_dwordx4 v[28:31], v[0:1], off
	global_load_dwordx4 v[32:35], v[2:3], off
	ds_bpermute_b32 v0, v44, v52 offset:32
	ds_bpermute_b32 v2, v44, v53 offset:32
	v_ashrrev_i32_e32 v59, 31, v58
	v_ashrrev_i32_e32 v61, 31, v60
	v_lshlrev_b64 v[58:59], 7, v[58:59]
	s_waitcnt lgkmcnt(1)
	v_ashrrev_i32_e32 v1, 31, v0
	s_waitcnt lgkmcnt(0)
	v_ashrrev_i32_e32 v3, 31, v2
	v_lshlrev_b64 v[0:1], 7, v[0:1]
	v_lshlrev_b64 v[2:3], 7, v[2:3]
	v_lshl_add_u64 v[0:1], v[42:43], 0, v[0:1]
	v_lshl_add_u64 v[2:3], v[42:43], 0, v[2:3]
	global_load_dwordx4 v[20:23], v[0:1], off
	global_load_dwordx4 v[36:39], v[2:3], off
	ds_bpermute_b32 v0, v44, v52 offset:64
	ds_bpermute_b32 v2, v44, v53 offset:64
	v_lshlrev_b64 v[60:61], 7, v[60:61]
	v_lshl_add_u64 v[68:69], v[42:43], 0, v[58:59]
	v_lshl_add_u64 v[70:71], v[42:43], 0, v[60:61]
	s_waitcnt lgkmcnt(1)
	v_ashrrev_i32_e32 v1, 31, v0
	s_waitcnt lgkmcnt(0)
	v_ashrrev_i32_e32 v3, 31, v2
	v_lshlrev_b64 v[0:1], 7, v[0:1]
	v_lshlrev_b64 v[2:3], 7, v[2:3]
	v_lshl_add_u64 v[0:1], v[42:43], 0, v[0:1]
	v_lshl_add_u64 v[2:3], v[42:43], 0, v[2:3]
	global_load_dwordx4 v[16:19], v[0:1], off
	global_load_dwordx4 v[24:27], v[2:3], off
	global_load_dwordx4 v[8:11], v40, s[2:3] offset:16
	s_waitcnt vmcnt(6)
	v_cvt_f32_i32_sdwa v74, sext(v29) dst_sel:DWORD dst_unused:UNUSED_PAD src0_sel:BYTE_1
	global_load_dwordx4 v[0:3], v40, s[2:3]
	global_load_dwordx4 v[12:15], v40, s[2:3] offset:32
	global_load_dwordx4 v[4:7], v40, s[2:3] offset:48
	v_or3_b32 v40, v56, v54, v55
	ds_bpermute_b32 v54, v44, v52 offset:96
	ds_bpermute_b32 v56, v44, v53 offset:96
	s_waitcnt vmcnt(8)
	v_dot4c_i32_i8_e32 v63, v28, v32
	v_dot4c_i32_i8_e32 v63, v29, v33
	v_dot4c_i32_i8_e32 v63, v30, v34
	s_waitcnt lgkmcnt(1)
	v_ashrrev_i32_e32 v55, 31, v54
	s_waitcnt lgkmcnt(0)
	v_ashrrev_i32_e32 v57, 31, v56
	v_lshlrev_b64 v[54:55], 7, v[54:55]
	v_lshlrev_b64 v[56:57], 7, v[56:57]
	v_lshl_add_u64 v[64:65], v[42:43], 0, v[54:55]
	v_lshl_add_u64 v[66:67], v[42:43], 0, v[56:57]
	global_load_dwordx4 v[54:57], v[64:65], off
	global_load_dwordx4 v[58:61], v[66:67], off
	s_waitcnt vmcnt(8)
	v_dot4c_i32_i8_e32 v72, v20, v36
	v_dot4c_i32_i8_e32 v72, v21, v37
	v_dot4c_i32_i8_e32 v72, v22, v38
	v_cvt_f32_i32_sdwa v32, sext(v28) dst_sel:DWORD dst_unused:UNUSED_PAD src0_sel:BYTE_0
	v_cvt_f32_i32_sdwa v64, sext(v29) dst_sel:DWORD dst_unused:UNUSED_PAD src0_sel:BYTE_0
	v_cvt_f32_i32_sdwa v65, sext(v30) dst_sel:DWORD dst_unused:UNUSED_PAD src0_sel:BYTE_0
	v_cvt_f32_i32_sdwa v66, sext(v31) dst_sel:DWORD dst_unused:UNUSED_PAD src0_sel:BYTE_0
	v_cvt_f32_i32_sdwa v67, sext(v28) dst_sel:DWORD dst_unused:UNUSED_PAD src0_sel:BYTE_1
	v_cvt_f32_i32_sdwa v75, sext(v30) dst_sel:DWORD dst_unused:UNUSED_PAD src0_sel:BYTE_1
	v_cvt_f32_i32_sdwa v76, sext(v31) dst_sel:DWORD dst_unused:UNUSED_PAD src0_sel:BYTE_1
	v_cvt_f32_i32_sdwa v77, sext(v28) dst_sel:DWORD dst_unused:UNUSED_PAD src0_sel:BYTE_2
	v_cvt_f32_i32_sdwa v78, sext(v29) dst_sel:DWORD dst_unused:UNUSED_PAD src0_sel:BYTE_2
	v_cvt_f32_i32_sdwa v79, sext(v30) dst_sel:DWORD dst_unused:UNUSED_PAD src0_sel:BYTE_2
	v_cvt_f32_i32_sdwa v80, sext(v31) dst_sel:DWORD dst_unused:UNUSED_PAD src0_sel:BYTE_2
	v_cvt_f32_i32_sdwa v81, sext(v28) dst_sel:DWORD dst_unused:UNUSED_PAD src0_sel:BYTE_3
	v_cvt_f32_i32_sdwa v82, sext(v29) dst_sel:DWORD dst_unused:UNUSED_PAD src0_sel:BYTE_3
	v_cvt_f32_i32_sdwa v83, sext(v30) dst_sel:DWORD dst_unused:UNUSED_PAD src0_sel:BYTE_3
	v_cvt_f32_i32_sdwa v84, sext(v31) dst_sel:DWORD dst_unused:UNUSED_PAD src0_sel:BYTE_3
	v_cvt_f32_i32_sdwa v36, sext(v20) dst_sel:DWORD dst_unused:UNUSED_PAD src0_sel:BYTE_0
	v_cvt_f32_i32_sdwa v85, sext(v21) dst_sel:DWORD dst_unused:UNUSED_PAD src0_sel:BYTE_0
	v_cvt_f32_i32_sdwa v86, sext(v22) dst_sel:DWORD dst_unused:UNUSED_PAD src0_sel:BYTE_0
	v_cvt_f32_i32_sdwa v87, sext(v23) dst_sel:DWORD dst_unused:UNUSED_PAD src0_sel:BYTE_0
	v_cvt_f32_i32_sdwa v88, sext(v20) dst_sel:DWORD dst_unused:UNUSED_PAD src0_sel:BYTE_1
	v_dot4c_i32_i8_e32 v63, v31, v35
	v_cvt_f32_i32_sdwa v33, sext(v21) dst_sel:DWORD dst_unused:UNUSED_PAD src0_sel:BYTE_1
	v_cvt_f32_i32_sdwa v34, sext(v22) dst_sel:DWORD dst_unused:UNUSED_PAD src0_sel:BYTE_1
	v_cvt_f32_i32_sdwa v35, sext(v23) dst_sel:DWORD dst_unused:UNUSED_PAD src0_sel:BYTE_1
	v_cvt_f32_i32_sdwa v89, sext(v20) dst_sel:DWORD dst_unused:UNUSED_PAD src0_sel:BYTE_2
	v_cvt_f32_i32_sdwa v90, sext(v21) dst_sel:DWORD dst_unused:UNUSED_PAD src0_sel:BYTE_2
	v_cvt_f32_i32_sdwa v91, sext(v22) dst_sel:DWORD dst_unused:UNUSED_PAD src0_sel:BYTE_2
	v_cvt_f32_i32_sdwa v92, sext(v23) dst_sel:DWORD dst_unused:UNUSED_PAD src0_sel:BYTE_2
	v_cvt_f32_i32_sdwa v93, sext(v20) dst_sel:DWORD dst_unused:UNUSED_PAD src0_sel:BYTE_3
	v_dot4c_i32_i8_e32 v72, v23, v39
	v_cvt_f32_i32_sdwa v37, sext(v21) dst_sel:DWORD dst_unused:UNUSED_PAD src0_sel:BYTE_3
	v_cvt_f32_i32_sdwa v38, sext(v22) dst_sel:DWORD dst_unused:UNUSED_PAD src0_sel:BYTE_3
	v_cvt_f32_i32_sdwa v39, sext(v23) dst_sel:DWORD dst_unused:UNUSED_PAD src0_sel:BYTE_3
	global_load_dwordx4 v[20:23], v[68:69], off
	global_load_dwordx4 v[28:31], v[70:71], off
	s_waitcnt vmcnt(8)
	v_dot4c_i32_i8_e32 v73, v16, v24
	v_cvt_f32_i32_sdwa v24, sext(v16) dst_sel:DWORD dst_unused:UNUSED_PAD src0_sel:BYTE_0
	v_dot4c_i32_i8_e32 v73, v17, v25
	v_cvt_f32_i32_sdwa v25, sext(v17) dst_sel:DWORD dst_unused:UNUSED_PAD src0_sel:BYTE_0
	v_dot4c_i32_i8_e32 v73, v18, v26
	v_cvt_f32_i32_sdwa v26, sext(v18) dst_sel:DWORD dst_unused:UNUSED_PAD src0_sel:BYTE_0
	v_dot4c_i32_i8_e32 v73, v19, v27
	v_cvt_f32_i32_sdwa v27, sext(v19) dst_sel:DWORD dst_unused:UNUSED_PAD src0_sel:BYTE_0
	v_cvt_f32_i32_sdwa v68, sext(v16) dst_sel:DWORD dst_unused:UNUSED_PAD src0_sel:BYTE_1
	v_cmp_eq_u32_e64 s[2:3], 2, v51
	v_mov_b32_e32 v70, v41
	s_waitcnt vmcnt(6)
	v_fma_f32 v32, v32, v0, 0
	v_fma_f32 v36, v36, v0, 0
	v_fmac_f32_e32 v32, v64, v8
	v_fmac_f32_e32 v36, v85, v8
	s_waitcnt vmcnt(5)
	v_fmac_f32_e32 v32, v65, v12
	v_fmac_f32_e32 v36, v86, v12
	s_waitcnt vmcnt(4)
	v_fmac_f32_e32 v32, v66, v4
	v_fmac_f32_e32 v36, v87, v4
	v_fmac_f32_e32 v32, v67, v1
	v_fmac_f32_e32 v36, v88, v1
	v_fmac_f32_e32 v32, v74, v9
	v_fmac_f32_e32 v36, v33, v9
	v_fmac_f32_e32 v32, v75, v13
	v_fmac_f32_e32 v36, v34, v13
	v_fmac_f32_e32 v32, v76, v5
	v_fmac_f32_e32 v36, v35, v5
	v_fmac_f32_e32 v32, v77, v2
	v_fmac_f32_e32 v36, v89, v2
	v_fmac_f32_e32 v32, v78, v10
	v_fmac_f32_e32 v36, v90, v10
	v_fmac_f32_e32 v32, v79, v14
	v_fmac_f32_e32 v36, v91, v14
	v_fmac_f32_e32 v32, v80, v6
	v_fma_f32 v69, v24, v0, 0
	v_add_u32_dpp v24, v63, v63 quad_perm:[1,0,3,2] row_mask:0xf bank_mask:0xf bound_ctrl:1
	v_fmac_f32_e32 v36, v92, v6
	v_fmac_f32_e32 v32, v81, v3
	v_add_u32_dpp v63, v72, v72 quad_perm:[1,0,3,2] row_mask:0xf bank_mask:0xf bound_ctrl:1
	v_add_u32_dpp v24, v24, v24 quad_perm:[2,3,0,1] row_mask:0xf bank_mask:0xf bound_ctrl:1
	v_fmac_f32_e32 v36, v93, v3
	v_fmac_f32_e32 v32, v82, v11
	v_fmac_f32_e32 v69, v25, v8
	v_add_u32_dpp v25, v63, v63 quad_perm:[2,3,0,1] row_mask:0xf bank_mask:0xf bound_ctrl:1
	v_add_u32_dpp v24, v24, v24 row_half_mirror row_mask:0xf bank_mask:0xf bound_ctrl:1
	v_fmac_f32_e32 v36, v37, v11
	v_fmac_f32_e32 v32, v83, v15
	v_add_u32_dpp v25, v25, v25 row_half_mirror row_mask:0xf bank_mask:0xf bound_ctrl:1
	v_cndmask_b32_e32 v24, 0, v24, vcc
	v_fmac_f32_e32 v36, v38, v15
	v_fmac_f32_e32 v32, v84, v7
	v_cndmask_b32_e64 v64, v24, v25, s[0:1]
	v_fmac_f32_e32 v36, v39, v7
	v_add_f32_dpp v24, v32, v32 quad_perm:[1,0,3,2] row_mask:0xf bank_mask:0xf bound_ctrl:1
	v_fmac_f32_e32 v69, v26, v12
	v_add_f32_dpp v25, v36, v36 quad_perm:[1,0,3,2] row_mask:0xf bank_mask:0xf bound_ctrl:1
	v_add_f32_dpp v24, v24, v24 quad_perm:[2,3,0,1] row_mask:0xf bank_mask:0xf bound_ctrl:1
	v_fmac_f32_e32 v69, v27, v4
	v_add_f32_dpp v25, v25, v25 quad_perm:[2,3,0,1] row_mask:0xf bank_mask:0xf bound_ctrl:1
	v_add_f32_dpp v24, v24, v24 row_half_mirror row_mask:0xf bank_mask:0xf bound_ctrl:1
	v_cndmask_b32_e32 v24, 0, v24, vcc
	v_add_f32_dpp v25, v25, v25 row_half_mirror row_mask:0xf bank_mask:0xf bound_ctrl:1
	v_cndmask_b32_e64 v36, v24, v25, s[0:1]
	v_cvt_f32_i32_sdwa v24, sext(v17) dst_sel:DWORD dst_unused:UNUSED_PAD src0_sel:BYTE_1
	v_cvt_f32_i32_sdwa v25, sext(v18) dst_sel:DWORD dst_unused:UNUSED_PAD src0_sel:BYTE_1
	v_fmac_f32_e32 v69, v68, v1
	v_cvt_f32_i32_sdwa v26, sext(v19) dst_sel:DWORD dst_unused:UNUSED_PAD src0_sel:BYTE_1
	v_fmac_f32_e32 v69, v24, v9
	v_fmac_f32_e32 v69, v25, v13
	v_cvt_f32_i32_sdwa v25, sext(v16) dst_sel:DWORD dst_unused:UNUSED_PAD src0_sel:BYTE_2
	v_cvt_f32_i32_sdwa v32, sext(v17) dst_sel:DWORD dst_unused:UNUSED_PAD src0_sel:BYTE_2
	ds_bpermute_b32 v24, v44, v53 offset:160
	v_fmac_f32_e32 v69, v26, v5
	v_ashrrev_i32_e32 v63, 31, v62
	v_cvt_f32_i32_sdwa v34, sext(v18) dst_sel:DWORD dst_unused:UNUSED_PAD src0_sel:BYTE_2
	v_lshlrev_b64 v[26:27], 7, v[62:63]
	v_fmac_f32_e32 v69, v25, v2
	v_cvt_f32_i32_sdwa v35, sext(v19) dst_sel:DWORD dst_unused:UNUSED_PAD src0_sel:BYTE_2
	v_fmac_f32_e32 v69, v32, v10
	v_lshl_add_u64 v[32:33], v[42:43], 0, v[26:27]
	v_cvt_f32_i32_sdwa v26, sext(v16) dst_sel:DWORD dst_unused:UNUSED_PAD src0_sel:BYTE_3
	v_cvt_f32_i32_sdwa v27, sext(v17) dst_sel:DWORD dst_unused:UNUSED_PAD src0_sel:BYTE_3
	v_fmac_f32_e32 v69, v34, v14
	v_cvt_f32_i32_sdwa v37, sext(v18) dst_sel:DWORD dst_unused:UNUSED_PAD src0_sel:BYTE_3
	s_waitcnt lgkmcnt(0)
	v_ashrrev_i32_e32 v25, 31, v24
	v_fmac_f32_e32 v69, v35, v6
	v_cvt_f32_i32_sdwa v38, sext(v19) dst_sel:DWORD dst_unused:UNUSED_PAD src0_sel:BYTE_3
	v_lshlrev_b64 v[16:17], 7, v[24:25]
	v_fmac_f32_e32 v69, v26, v3
	v_lshl_add_u64 v[34:35], v[42:43], 0, v[16:17]
	v_fmac_f32_e32 v69, v27, v11
	global_load_dwordx4 v[16:19], v[32:33], off
	global_load_dwordx4 v[24:27], v[34:35], off
	v_add_u32_dpp v33, v73, v73 quad_perm:[1,0,3,2] row_mask:0xf bank_mask:0xf bound_ctrl:1
	v_fmac_f32_e32 v69, v37, v15
	v_fmac_f32_e32 v69, v38, v7
	v_add_u32_dpp v33, v33, v33 quad_perm:[2,3,0,1] row_mask:0xf bank_mask:0xf bound_ctrl:1
	s_waitcnt vmcnt(5)
	v_cvt_f32_i32_sdwa v35, sext(v57) dst_sel:DWORD dst_unused:UNUSED_PAD src0_sel:BYTE_0
	v_add_f32_dpp v34, v69, v69 quad_perm:[1,0,3,2] row_mask:0xf bank_mask:0xf bound_ctrl:1
	v_add_u32_dpp v33, v33, v33 row_half_mirror row_mask:0xf bank_mask:0xf bound_ctrl:1
	v_cndmask_b32_e64 v63, v64, v33, s[2:3]
	v_cvt_f32_i32_sdwa v33, sext(v54) dst_sel:DWORD dst_unused:UNUSED_PAD src0_sel:BYTE_0
	v_add_f32_dpp v34, v34, v34 quad_perm:[2,3,0,1] row_mask:0xf bank_mask:0xf bound_ctrl:1
	v_mov_b32_e32 v64, v41
	s_waitcnt vmcnt(4)
	v_dot4c_i32_i8_e32 v64, v54, v58
	v_add_f32_dpp v34, v34, v34 row_half_mirror row_mask:0xf bank_mask:0xf bound_ctrl:1
	v_cndmask_b32_e64 v62, v36, v34, s[2:3]
	v_dot4c_i32_i8_e32 v64, v55, v59
	v_cvt_f32_i32_sdwa v34, sext(v55) dst_sel:DWORD dst_unused:UNUSED_PAD src0_sel:BYTE_0
	v_dot4c_i32_i8_e32 v64, v56, v60
	v_fma_f32 v60, v33, v0, 0
	v_cvt_f32_i32_sdwa v33, sext(v56) dst_sel:DWORD dst_unused:UNUSED_PAD src0_sel:BYTE_0
	v_fmac_f32_e32 v60, v34, v8
	v_cvt_f32_i32_sdwa v34, sext(v54) dst_sel:DWORD dst_unused:UNUSED_PAD src0_sel:BYTE_1
	v_cvt_f32_i32_sdwa v36, sext(v57) dst_sel:DWORD dst_unused:UNUSED_PAD src0_sel:BYTE_1
	v_fmac_f32_e32 v60, v33, v12
	v_cvt_f32_i32_sdwa v33, sext(v55) dst_sel:DWORD dst_unused:UNUSED_PAD src0_sel:BYTE_1
	v_fmac_f32_e32 v60, v35, v4
	v_cvt_f32_i32_sdwa v35, sext(v56) dst_sel:DWORD dst_unused:UNUSED_PAD src0_sel:BYTE_1
	v_fmac_f32_e32 v60, v34, v1
	v_fmac_f32_e32 v60, v33, v9
	v_cvt_f32_i32_sdwa v37, sext(v57) dst_sel:DWORD dst_unused:UNUSED_PAD src0_sel:BYTE_2
	v_fmac_f32_e32 v60, v35, v13
	v_cvt_f32_i32_sdwa v35, sext(v54) dst_sel:DWORD dst_unused:UNUSED_PAD src0_sel:BYTE_2
	v_fmac_f32_e32 v60, v36, v5
	v_cvt_f32_i32_sdwa v36, sext(v55) dst_sel:DWORD dst_unused:UNUSED_PAD src0_sel:BYTE_2
	ds_bpermute_b32 v32, v44, v52 offset:192
	v_fmac_f32_e32 v60, v35, v2
	ds_bpermute_b32 v34, v44, v53 offset:192
	v_fmac_f32_e32 v60, v36, v10
	v_cvt_f32_i32_sdwa v36, sext(v56) dst_sel:DWORD dst_unused:UNUSED_PAD src0_sel:BYTE_2
	v_cvt_f32_i32_sdwa v56, sext(v56) dst_sel:DWORD dst_unused:UNUSED_PAD src0_sel:BYTE_3
	v_dot4c_i32_i8_e32 v64, v57, v61
	v_cvt_f32_i32_sdwa v57, sext(v57) dst_sel:DWORD dst_unused:UNUSED_PAD src0_sel:BYTE_3
	v_fmac_f32_e32 v60, v36, v14
	v_cvt_f32_i32_sdwa v36, sext(v54) dst_sel:DWORD dst_unused:UNUSED_PAD src0_sel:BYTE_3
	v_fmac_f32_e32 v60, v37, v6
	v_cvt_f32_i32_sdwa v37, sext(v55) dst_sel:DWORD dst_unused:UNUSED_PAD src0_sel:BYTE_3
	s_waitcnt lgkmcnt(1)
	v_ashrrev_i32_e32 v33, 31, v32
	v_fmac_f32_e32 v60, v36, v3
	v_lshlrev_b64 v[32:33], 7, v[32:33]
	s_waitcnt lgkmcnt(0)
	v_ashrrev_i32_e32 v35, 31, v34
	v_fmac_f32_e32 v60, v37, v11
	v_lshl_add_u64 v[58:59], v[42:43], 0, v[32:33]
	v_lshlrev_b64 v[32:33], 7, v[34:35]
	v_fmac_f32_e32 v60, v56, v15
	v_lshl_add_u64 v[54:55], v[42:43], 0, v[32:33]
	v_fmac_f32_e32 v60, v57, v7
	global_load_dwordx4 v[32:35], v[58:59], off
	global_load_dwordx4 v[36:39], v[54:55], off
	v_add_f32_dpp v55, v60, v60 quad_perm:[1,0,3,2] row_mask:0xf bank_mask:0xf bound_ctrl:1
	v_add_u32_dpp v54, v64, v64 quad_perm:[1,0,3,2] row_mask:0xf bank_mask:0xf bound_ctrl:1
	s_waitcnt vmcnt(5)
	v_cvt_f32_i32_sdwa v58, sext(v22) dst_sel:DWORD dst_unused:UNUSED_PAD src0_sel:BYTE_0
	v_add_f32_dpp v55, v55, v55 quad_perm:[2,3,0,1] row_mask:0xf bank_mask:0xf bound_ctrl:1
	v_add_u32_dpp v54, v54, v54 quad_perm:[2,3,0,1] row_mask:0xf bank_mask:0xf bound_ctrl:1
	ds_bpermute_b32 v52, v44, v52 offset:224
	v_add_f32_dpp v55, v55, v55 row_half_mirror row_mask:0xf bank_mask:0xf bound_ctrl:1
	v_cndmask_b32_e64 v56, v62, v55, s[4:5]
	v_cvt_f32_i32_sdwa v55, sext(v20) dst_sel:DWORD dst_unused:UNUSED_PAD src0_sel:BYTE_0
	v_add_u32_dpp v54, v54, v54 row_half_mirror row_mask:0xf bank_mask:0xf bound_ctrl:1
	v_cndmask_b32_e64 v57, v63, v54, s[4:5]
	v_cvt_f32_i32_sdwa v54, sext(v21) dst_sel:DWORD dst_unused:UNUSED_PAD src0_sel:BYTE_0
	v_fma_f32 v59, v55, v0, 0
	v_cvt_f32_i32_sdwa v55, sext(v23) dst_sel:DWORD dst_unused:UNUSED_PAD src0_sel:BYTE_0
	v_cvt_f32_i32_sdwa v60, sext(v20) dst_sel:DWORD dst_unused:UNUSED_PAD src0_sel:BYTE_3
	v_fmac_f32_e32 v59, v54, v8
	v_fmac_f32_e32 v59, v58, v12
	v_cvt_f32_i32_sdwa v54, sext(v20) dst_sel:DWORD dst_unused:UNUSED_PAD src0_sel:BYTE_1
	v_fmac_f32_e32 v59, v55, v4
	v_cvt_f32_i32_sdwa v55, sext(v21) dst_sel:DWORD dst_unused:UNUSED_PAD src0_sel:BYTE_1
	v_cvt_f32_i32_sdwa v58, sext(v22) dst_sel:DWORD dst_unused:UNUSED_PAD src0_sel:BYTE_1
	v_fmac_f32_e32 v59, v54, v1
	v_cvt_f32_i32_sdwa v54, sext(v23) dst_sel:DWORD dst_unused:UNUSED_PAD src0_sel:BYTE_1
	v_fmac_f32_e32 v59, v55, v9
	v_cvt_f32_i32_sdwa v55, sext(v20) dst_sel:DWORD dst_unused:UNUSED_PAD src0_sel:BYTE_2
	v_fmac_f32_e32 v59, v58, v13
	v_cvt_f32_i32_sdwa v58, sext(v21) dst_sel:DWORD dst_unused:UNUSED_PAD src0_sel:BYTE_2
	v_fmac_f32_e32 v59, v54, v5
	v_fmac_f32_e32 v59, v55, v2
	v_cvt_f32_i32_sdwa v55, sext(v22) dst_sel:DWORD dst_unused:UNUSED_PAD src0_sel:BYTE_2
	v_fmac_f32_e32 v59, v58, v10
	v_cvt_f32_i32_sdwa v58, sext(v23) dst_sel:DWORD dst_unused:UNUSED_PAD src0_sel:BYTE_2
	ds_bpermute_b32 v54, v44, v53 offset:224
	v_fmac_f32_e32 v59, v55, v14
	s_waitcnt lgkmcnt(1)
	v_ashrrev_i32_e32 v53, 31, v52
	v_fmac_f32_e32 v59, v58, v6
	v_mov_b32_e32 v58, v41
	s_waitcnt vmcnt(4)
	v_dot4c_i32_i8_e32 v58, v20, v28
	v_lshlrev_b64 v[52:53], 7, v[52:53]
	s_waitcnt lgkmcnt(0)
	v_ashrrev_i32_e32 v55, 31, v54
	v_dot4c_i32_i8_e32 v58, v21, v29
	v_lshl_add_u64 v[52:53], v[42:43], 0, v[52:53]
	v_lshlrev_b64 v[54:55], 7, v[54:55]
	v_dot4c_i32_i8_e32 v58, v22, v30
	v_lshl_add_u64 v[54:55], v[42:43], 0, v[54:55]
	v_dot4c_i32_i8_e32 v58, v23, v31
	v_cvt_f32_i32_sdwa v61, sext(v21) dst_sel:DWORD dst_unused:UNUSED_PAD src0_sel:BYTE_3
	v_cvt_f32_i32_sdwa v62, sext(v22) dst_sel:DWORD dst_unused:UNUSED_PAD src0_sel:BYTE_3
	v_cvt_f32_i32_sdwa v63, sext(v23) dst_sel:DWORD dst_unused:UNUSED_PAD src0_sel:BYTE_3
	global_load_dwordx4 v[20:23], v[52:53], off
	global_load_dwordx4 v[28:31], v[54:55], off
	v_mov_b32_e32 v54, v41
	s_waitcnt vmcnt(4)
	v_dot4c_i32_i8_e32 v54, v16, v24
	v_cvt_f32_i32_sdwa v24, sext(v16) dst_sel:DWORD dst_unused:UNUSED_PAD src0_sel:BYTE_0
	v_fmac_f32_e32 v59, v60, v3
	v_dot4c_i32_i8_e32 v54, v17, v25
	v_cvt_f32_i32_sdwa v25, sext(v17) dst_sel:DWORD dst_unused:UNUSED_PAD src0_sel:BYTE_0
	v_fmac_f32_e32 v59, v61, v11
	v_dot4c_i32_i8_e32 v54, v18, v26
	v_cvt_f32_i32_sdwa v26, sext(v18) dst_sel:DWORD dst_unused:UNUSED_PAD src0_sel:BYTE_0
	v_fmac_f32_e32 v59, v62, v15
	v_cvt_f32_i32_sdwa v55, sext(v19) dst_sel:DWORD dst_unused:UNUSED_PAD src0_sel:BYTE_0
	v_fmac_f32_e32 v59, v63, v7
	v_fma_f32 v24, v24, v0, 0
	v_fmac_f32_e32 v24, v25, v8
	v_add_f32_dpp v53, v59, v59 quad_perm:[1,0,3,2] row_mask:0xf bank_mask:0xf bound_ctrl:1
	v_cvt_f32_i32_sdwa v25, sext(v16) dst_sel:DWORD dst_unused:UNUSED_PAD src0_sel:BYTE_1
	v_fmac_f32_e32 v24, v26, v12
	v_add_f32_dpp v53, v53, v53 quad_perm:[2,3,0,1] row_mask:0xf bank_mask:0xf bound_ctrl:1
	v_cvt_f32_i32_sdwa v26, sext(v17) dst_sel:DWORD dst_unused:UNUSED_PAD src0_sel:BYTE_1
	v_fmac_f32_e32 v24, v55, v4
	v_add_f32_dpp v53, v53, v53 row_half_mirror row_mask:0xf bank_mask:0xf bound_ctrl:1
	v_cvt_f32_i32_sdwa v55, sext(v18) dst_sel:DWORD dst_unused:UNUSED_PAD src0_sel:BYTE_1
	v_cndmask_b32_e64 v53, v56, v53, s[6:7]
	v_cvt_f32_i32_sdwa v56, sext(v19) dst_sel:DWORD dst_unused:UNUSED_PAD src0_sel:BYTE_1
	v_fmac_f32_e32 v24, v25, v1
	v_cvt_f32_i32_sdwa v25, sext(v16) dst_sel:DWORD dst_unused:UNUSED_PAD src0_sel:BYTE_2
	v_fmac_f32_e32 v24, v26, v9
	v_cvt_f32_i32_sdwa v26, sext(v17) dst_sel:DWORD dst_unused:UNUSED_PAD src0_sel:BYTE_2
	v_fmac_f32_e32 v24, v55, v13
	v_cvt_f32_i32_sdwa v55, sext(v18) dst_sel:DWORD dst_unused:UNUSED_PAD src0_sel:BYTE_2
	v_fmac_f32_e32 v24, v56, v5
	v_cvt_f32_i32_sdwa v56, sext(v19) dst_sel:DWORD dst_unused:UNUSED_PAD src0_sel:BYTE_2
	v_fmac_f32_e32 v24, v25, v2
	v_cvt_f32_i32_sdwa v16, sext(v16) dst_sel:DWORD dst_unused:UNUSED_PAD src0_sel:BYTE_3
	v_fmac_f32_e32 v24, v26, v10
	v_cvt_f32_i32_sdwa v17, sext(v17) dst_sel:DWORD dst_unused:UNUSED_PAD src0_sel:BYTE_3
	v_fmac_f32_e32 v24, v55, v14
	v_cvt_f32_i32_sdwa v18, sext(v18) dst_sel:DWORD dst_unused:UNUSED_PAD src0_sel:BYTE_3
	v_fmac_f32_e32 v24, v56, v6
	v_cvt_f32_i32_sdwa v25, sext(v19) dst_sel:DWORD dst_unused:UNUSED_PAD src0_sel:BYTE_3
	v_fmac_f32_e32 v24, v16, v3
	v_fmac_f32_e32 v24, v17, v11
	v_fmac_f32_e32 v24, v18, v15
	v_fmac_f32_e32 v24, v25, v7
	v_dot4c_i32_i8_e32 v54, v19, v27
	s_waitcnt vmcnt(3)
	v_cvt_f32_i32_sdwa v19, sext(v32) dst_sel:DWORD dst_unused:UNUSED_PAD src0_sel:BYTE_0
	v_add_f32_dpp v17, v24, v24 quad_perm:[1,0,3,2] row_mask:0xf bank_mask:0xf bound_ctrl:1
	v_cvt_f32_i32_sdwa v24, sext(v33) dst_sel:DWORD dst_unused:UNUSED_PAD src0_sel:BYTE_0
	v_cvt_f32_i32_sdwa v25, sext(v34) dst_sel:DWORD dst_unused:UNUSED_PAD src0_sel:BYTE_0
	v_cvt_f32_i32_sdwa v26, sext(v35) dst_sel:DWORD dst_unused:UNUSED_PAD src0_sel:BYTE_0
	v_fma_f32 v19, v19, v0, 0
	v_fmac_f32_e32 v19, v24, v8
	v_cvt_f32_i32_sdwa v24, sext(v32) dst_sel:DWORD dst_unused:UNUSED_PAD src0_sel:BYTE_1
	v_fmac_f32_e32 v19, v25, v12
	v_cvt_f32_i32_sdwa v25, sext(v33) dst_sel:DWORD dst_unused:UNUSED_PAD src0_sel:BYTE_1
	v_fmac_f32_e32 v19, v26, v4
	v_cvt_f32_i32_sdwa v26, sext(v34) dst_sel:DWORD dst_unused:UNUSED_PAD src0_sel:BYTE_1
	v_cvt_f32_i32_sdwa v27, sext(v35) dst_sel:DWORD dst_unused:UNUSED_PAD src0_sel:BYTE_1
	v_fmac_f32_e32 v19, v24, v1
	v_cvt_f32_i32_sdwa v24, sext(v32) dst_sel:DWORD dst_unused:UNUSED_PAD src0_sel:BYTE_2
	v_fmac_f32_e32 v19, v25, v9
	v_cvt_f32_i32_sdwa v25, sext(v33) dst_sel:DWORD dst_unused:UNUSED_PAD src0_sel:BYTE_2
	v_fmac_f32_e32 v19, v26, v13
	v_cvt_f32_i32_sdwa v26, sext(v34) dst_sel:DWORD dst_unused:UNUSED_PAD src0_sel:BYTE_2
	v_fmac_f32_e32 v19, v27, v5
	v_cvt_f32_i32_sdwa v27, sext(v35) dst_sel:DWORD dst_unused:UNUSED_PAD src0_sel:BYTE_2
	v_fmac_f32_e32 v19, v24, v2
	v_cvt_f32_i32_sdwa v24, sext(v32) dst_sel:DWORD dst_unused:UNUSED_PAD src0_sel:BYTE_3
	v_fmac_f32_e32 v19, v25, v10
	v_cvt_f32_i32_sdwa v25, sext(v33) dst_sel:DWORD dst_unused:UNUSED_PAD src0_sel:BYTE_3
	v_fmac_f32_e32 v19, v26, v14
	v_cvt_f32_i32_sdwa v26, sext(v34) dst_sel:DWORD dst_unused:UNUSED_PAD src0_sel:BYTE_3
	v_fmac_f32_e32 v19, v27, v6
	v_cvt_f32_i32_sdwa v27, sext(v35) dst_sel:DWORD dst_unused:UNUSED_PAD src0_sel:BYTE_3
	v_fmac_f32_e32 v19, v24, v3
	v_fmac_f32_e32 v19, v25, v11
	v_fmac_f32_e32 v19, v26, v15
	v_fmac_f32_e32 v19, v27, v7
	v_add_f32_dpp v17, v17, v17 quad_perm:[2,3,0,1] row_mask:0xf bank_mask:0xf bound_ctrl:1
	s_waitcnt vmcnt(1)
	v_cvt_f32_i32_sdwa v24, sext(v21) dst_sel:DWORD dst_unused:UNUSED_PAD src0_sel:BYTE_0
	v_add_f32_dpp v19, v19, v19 quad_perm:[1,0,3,2] row_mask:0xf bank_mask:0xf bound_ctrl:1
	v_add_f32_dpp v17, v17, v17 row_half_mirror row_mask:0xf bank_mask:0xf bound_ctrl:1
	v_cndmask_b32_e64 v17, v53, v17, s[8:9]
	v_add_f32_dpp v19, v19, v19 quad_perm:[2,3,0,1] row_mask:0xf bank_mask:0xf bound_ctrl:1
	v_cvt_f32_i32_sdwa v25, sext(v22) dst_sel:DWORD dst_unused:UNUSED_PAD src0_sel:BYTE_0
	v_cvt_f32_i32_sdwa v26, sext(v23) dst_sel:DWORD dst_unused:UNUSED_PAD src0_sel:BYTE_0
	v_add_f32_dpp v19, v19, v19 row_half_mirror row_mask:0xf bank_mask:0xf bound_ctrl:1
	v_cndmask_b32_e64 v17, v17, v19, s[10:11]
	v_cvt_f32_i32_sdwa v19, sext(v20) dst_sel:DWORD dst_unused:UNUSED_PAD src0_sel:BYTE_0
	v_mov_b32_e32 v18, v41
	v_dot4c_i32_i8_e32 v18, v32, v36
	v_dot4c_i32_i8_e32 v18, v33, v37
	v_fma_f32 v19, v19, v0, 0
	v_fmac_f32_e32 v19, v24, v8
	v_cvt_f32_i32_sdwa v24, sext(v20) dst_sel:DWORD dst_unused:UNUSED_PAD src0_sel:BYTE_1
	v_fmac_f32_e32 v19, v25, v12
	v_cvt_f32_i32_sdwa v25, sext(v21) dst_sel:DWORD dst_unused:UNUSED_PAD src0_sel:BYTE_1
	v_add_u32_dpp v52, v58, v58 quad_perm:[1,0,3,2] row_mask:0xf bank_mask:0xf bound_ctrl:1
	v_dot4c_i32_i8_e32 v18, v34, v38
	v_fmac_f32_e32 v19, v26, v4
	v_cvt_f32_i32_sdwa v26, sext(v22) dst_sel:DWORD dst_unused:UNUSED_PAD src0_sel:BYTE_1
	v_add_u32_dpp v52, v52, v52 quad_perm:[2,3,0,1] row_mask:0xf bank_mask:0xf bound_ctrl:1
	v_add_u32_dpp v16, v54, v54 quad_perm:[1,0,3,2] row_mask:0xf bank_mask:0xf bound_ctrl:1
	v_dot4c_i32_i8_e32 v18, v35, v39
	v_cvt_f32_i32_sdwa v27, sext(v23) dst_sel:DWORD dst_unused:UNUSED_PAD src0_sel:BYTE_1
	v_add_u32_dpp v52, v52, v52 row_half_mirror row_mask:0xf bank_mask:0xf bound_ctrl:1
	v_add_u32_dpp v16, v16, v16 quad_perm:[2,3,0,1] row_mask:0xf bank_mask:0xf bound_ctrl:1
	v_add_u32_dpp v18, v18, v18 quad_perm:[1,0,3,2] row_mask:0xf bank_mask:0xf bound_ctrl:1
	v_fmac_f32_e32 v19, v24, v1
	v_cvt_f32_i32_sdwa v24, sext(v20) dst_sel:DWORD dst_unused:UNUSED_PAD src0_sel:BYTE_2
	v_cndmask_b32_e64 v52, v57, v52, s[6:7]
	v_add_u32_dpp v16, v16, v16 row_half_mirror row_mask:0xf bank_mask:0xf bound_ctrl:1
	v_add_u32_dpp v18, v18, v18 quad_perm:[2,3,0,1] row_mask:0xf bank_mask:0xf bound_ctrl:1
	v_fmac_f32_e32 v19, v25, v9
	v_cvt_f32_i32_sdwa v25, sext(v21) dst_sel:DWORD dst_unused:UNUSED_PAD src0_sel:BYTE_2
	v_cndmask_b32_e64 v16, v52, v16, s[8:9]
	v_add_u32_dpp v18, v18, v18 row_half_mirror row_mask:0xf bank_mask:0xf bound_ctrl:1
	v_fmac_f32_e32 v19, v26, v13
	v_cvt_f32_i32_sdwa v26, sext(v22) dst_sel:DWORD dst_unused:UNUSED_PAD src0_sel:BYTE_2
	v_cndmask_b32_e64 v16, v16, v18, s[10:11]
	v_mov_b32_e32 v18, v41
	v_fmac_f32_e32 v19, v27, v5
	v_cvt_f32_i32_sdwa v27, sext(v23) dst_sel:DWORD dst_unused:UNUSED_PAD src0_sel:BYTE_2
	s_waitcnt vmcnt(0)
	v_dot4c_i32_i8_e32 v18, v20, v28
	v_fmac_f32_e32 v19, v24, v2
	v_cvt_f32_i32_sdwa v20, sext(v20) dst_sel:DWORD dst_unused:UNUSED_PAD src0_sel:BYTE_3
	v_dot4c_i32_i8_e32 v18, v21, v29
	v_fmac_f32_e32 v19, v25, v10
	v_cvt_f32_i32_sdwa v21, sext(v21) dst_sel:DWORD dst_unused:UNUSED_PAD src0_sel:BYTE_3
	v_dot4c_i32_i8_e32 v18, v22, v30
	v_fmac_f32_e32 v19, v26, v14
	v_cvt_f32_i32_sdwa v22, sext(v22) dst_sel:DWORD dst_unused:UNUSED_PAD src0_sel:BYTE_3
	v_fmac_f32_e32 v19, v27, v6
	v_cvt_f32_i32_sdwa v24, sext(v23) dst_sel:DWORD dst_unused:UNUSED_PAD src0_sel:BYTE_3
	v_fmac_f32_e32 v19, v20, v3
	v_fmac_f32_e32 v19, v21, v11
	v_fmac_f32_e32 v19, v22, v15
	v_fmac_f32_e32 v19, v24, v7
	v_dot4c_i32_i8_e32 v18, v23, v31
	ds_bpermute_b32 v58, v44, v50 offset:96
	v_add_f32_dpp v19, v19, v19 quad_perm:[1,0,3,2] row_mask:0xf bank_mask:0xf bound_ctrl:1
	s_waitcnt lgkmcnt(0)
	v_ashrrev_i32_e32 v59, 31, v58
	v_add_u32_dpp v18, v18, v18 quad_perm:[1,0,3,2] row_mask:0xf bank_mask:0xf bound_ctrl:1
	v_add_f32_dpp v19, v19, v19 quad_perm:[2,3,0,1] row_mask:0xf bank_mask:0xf bound_ctrl:1
	v_lshlrev_b64 v[58:59], 7, v[58:59]
	v_add_u32_dpp v18, v18, v18 quad_perm:[2,3,0,1] row_mask:0xf bank_mask:0xf bound_ctrl:1
	v_add_f32_dpp v19, v19, v19 row_half_mirror row_mask:0xf bank_mask:0xf bound_ctrl:1
	v_cndmask_b32_e64 v19, v17, v19, s[12:13]
	v_add_u32_dpp v18, v18, v18 row_half_mirror row_mask:0xf bank_mask:0xf bound_ctrl:1
	v_cndmask_b32_e64 v20, v16, v18, s[12:13]
	v_lshlrev_b64 v[16:17], 2, v[40:41]
	ds_bpermute_b32 v18, v44, v50
	s_add_u32 s21, s20, 2
	s_cmp_lt_u32 s20, 2
	s_cselect_b32 s21, s20, s21
	s_lshl_b32 s21, s21, 19
	s_add_u32 s22, s20, 10
	s_lshl_b32 s22, s22, 19
	s_sub_u32 s23, s20, 6
	s_lshl_b32 s23, s23, 19
	s_sub_u32 s23, s23, 0x262a80
	s_cmp_lt_u32 s20, 6
	s_cselect_b32 s22, s22, s23
	s_ashr_i32 s23, s22, 31
	s_add_u32 s18, s16, s22
	s_addc_u32 s19, s17, s23
	s_add_u32 s16, s16, s21
	s_addc_u32 s17, s17, 0
	v_lshl_add_u64 v[28:29], s[16:17], 0, v[16:17]
	v_lshl_add_u64 v[30:31], s[18:19], 0, v[16:17]
	ds_bpermute_b32 v16, v44, v49
	global_store_dword v[28:29], v20, off
	global_store_dword v[30:31], v19, off
	s_waitcnt lgkmcnt(1)
	v_ashrrev_i32_e32 v19, 31, v18
	v_lshlrev_b64 v[18:19], 7, v[18:19]
	s_waitcnt lgkmcnt(0)
	v_ashrrev_i32_e32 v17, 31, v16
	v_lshl_add_u64 v[18:19], v[42:43], 0, v[18:19]
	v_lshlrev_b64 v[16:17], 7, v[16:17]
	v_lshl_add_u64 v[16:17], v[42:43], 0, v[16:17]
	global_load_dwordx4 v[32:35], v[18:19], off
	global_load_dwordx4 v[36:39], v[16:17], off
	ds_bpermute_b32 v16, v44, v50 offset:32
	ds_bpermute_b32 v18, v44, v49 offset:32
	v_mov_b32_e32 v40, v41
	v_lshl_add_u64 v[58:59], v[42:43], 0, v[58:59]
	s_waitcnt lgkmcnt(1)
	v_ashrrev_i32_e32 v17, 31, v16
	v_lshlrev_b64 v[16:17], 7, v[16:17]
	s_waitcnt lgkmcnt(0)
	v_ashrrev_i32_e32 v19, 31, v18
	v_lshl_add_u64 v[16:17], v[42:43], 0, v[16:17]
	v_lshlrev_b64 v[18:19], 7, v[18:19]
	v_lshl_add_u64 v[18:19], v[42:43], 0, v[18:19]
	global_load_dwordx4 v[24:27], v[16:17], off
	global_load_dwordx4 v[52:55], v[18:19], off
	ds_bpermute_b32 v16, v44, v50 offset:64
	ds_bpermute_b32 v18, v44, v49 offset:64
	s_waitcnt lgkmcnt(1)
	v_ashrrev_i32_e32 v17, 31, v16
	v_lshlrev_b64 v[16:17], 7, v[16:17]
	s_waitcnt lgkmcnt(0)
	v_ashrrev_i32_e32 v19, 31, v18
	v_lshl_add_u64 v[56:57], v[42:43], 0, v[16:17]
	v_lshlrev_b64 v[16:17], 7, v[18:19]
	v_lshl_add_u64 v[60:61], v[42:43], 0, v[16:17]
	global_load_dwordx4 v[16:19], v[56:57], off
	global_load_dwordx4 v[20:23], v[60:61], off
	v_mov_b32_e32 v61, v41
	ds_bpermute_b32 v56, v44, v49 offset:96
	s_waitcnt lgkmcnt(0)
	v_ashrrev_i32_e32 v57, 31, v56
	s_waitcnt vmcnt(5)
	v_cvt_f32_i32_sdwa v60, sext(v32) dst_sel:DWORD dst_unused:UNUSED_PAD src0_sel:BYTE_2
	s_waitcnt vmcnt(4)
	v_dot4c_i32_i8_e32 v40, v32, v36
	v_cvt_f32_i32_sdwa v36, sext(v32) dst_sel:DWORD dst_unused:UNUSED_PAD src0_sel:BYTE_0
	v_dot4c_i32_i8_e32 v40, v33, v37
	v_cvt_f32_i32_sdwa v37, sext(v33) dst_sel:DWORD dst_unused:UNUSED_PAD src0_sel:BYTE_0
	v_dot4c_i32_i8_e32 v40, v34, v38
	v_cvt_f32_i32_sdwa v38, sext(v34) dst_sel:DWORD dst_unused:UNUSED_PAD src0_sel:BYTE_0
	v_fma_f32 v51, v36, v0, 0
	v_cvt_f32_i32_sdwa v36, sext(v35) dst_sel:DWORD dst_unused:UNUSED_PAD src0_sel:BYTE_0
	v_fmac_f32_e32 v51, v37, v8
	v_cvt_f32_i32_sdwa v37, sext(v32) dst_sel:DWORD dst_unused:UNUSED_PAD src0_sel:BYTE_1
	v_fmac_f32_e32 v51, v38, v12
	v_cvt_f32_i32_sdwa v38, sext(v33) dst_sel:DWORD dst_unused:UNUSED_PAD src0_sel:BYTE_1
	v_fmac_f32_e32 v51, v36, v4
	v_fmac_f32_e32 v51, v37, v1
	v_dot4c_i32_i8_e32 v40, v35, v39
	v_fmac_f32_e32 v51, v38, v9
	v_cvt_f32_i32_sdwa v38, sext(v34) dst_sel:DWORD dst_unused:UNUSED_PAD src0_sel:BYTE_1
	v_cvt_f32_i32_sdwa v39, sext(v35) dst_sel:DWORD dst_unused:UNUSED_PAD src0_sel:BYTE_1
	v_cvt_f32_i32_sdwa v32, sext(v32) dst_sel:DWORD dst_unused:UNUSED_PAD src0_sel:BYTE_3
	s_waitcnt vmcnt(2)
	v_dot4c_i32_i8_e32 v61, v24, v52
	v_fmac_f32_e32 v51, v38, v13
	v_cvt_f32_i32_sdwa v38, sext(v33) dst_sel:DWORD dst_unused:UNUSED_PAD src0_sel:BYTE_2
	v_fmac_f32_e32 v51, v39, v5
	v_cvt_f32_i32_sdwa v39, sext(v34) dst_sel:DWORD dst_unused:UNUSED_PAD src0_sel:BYTE_2
	v_fmac_f32_e32 v51, v60, v2
	v_cvt_f32_i32_sdwa v60, sext(v35) dst_sel:DWORD dst_unused:UNUSED_PAD src0_sel:BYTE_2
	v_fmac_f32_e32 v51, v38, v10
	v_cvt_f32_i32_sdwa v33, sext(v33) dst_sel:DWORD dst_unused:UNUSED_PAD src0_sel:BYTE_3
	v_fmac_f32_e32 v51, v39, v14
	v_cvt_f32_i32_sdwa v34, sext(v34) dst_sel:DWORD dst_unused:UNUSED_PAD src0_sel:BYTE_3
	v_fmac_f32_e32 v51, v60, v6
	v_fmac_f32_e32 v51, v32, v3
	v_cvt_f32_i32_sdwa v32, sext(v24) dst_sel:DWORD dst_unused:UNUSED_PAD src0_sel:BYTE_0
	v_fmac_f32_e32 v51, v33, v11
	v_cvt_f32_i32_sdwa v33, sext(v25) dst_sel:DWORD dst_unused:UNUSED_PAD src0_sel:BYTE_0
	v_fmac_f32_e32 v51, v34, v15
	v_cvt_f32_i32_sdwa v34, sext(v26) dst_sel:DWORD dst_unused:UNUSED_PAD src0_sel:BYTE_0
	v_cvt_f32_i32_sdwa v35, sext(v35) dst_sel:DWORD dst_unused:UNUSED_PAD src0_sel:BYTE_3
	v_fma_f32 v52, v32, v0, 0
	v_cvt_f32_i32_sdwa v32, sext(v27) dst_sel:DWORD dst_unused:UNUSED_PAD src0_sel:BYTE_0
	v_fmac_f32_e32 v52, v33, v8
	v_cvt_f32_i32_sdwa v33, sext(v24) dst_sel:DWORD dst_unused:UNUSED_PAD src0_sel:BYTE_1
	v_fmac_f32_e32 v52, v34, v12
	v_cvt_f32_i32_sdwa v34, sext(v25) dst_sel:DWORD dst_unused:UNUSED_PAD src0_sel:BYTE_1
	v_fmac_f32_e32 v51, v35, v7
	v_cvt_f32_i32_sdwa v35, sext(v26) dst_sel:DWORD dst_unused:UNUSED_PAD src0_sel:BYTE_1
	v_fmac_f32_e32 v52, v32, v4
	v_fmac_f32_e32 v52, v33, v1
	v_lshlrev_b64 v[36:37], 7, v[56:57]
	v_fmac_f32_e32 v52, v34, v9
	v_lshl_add_u64 v[56:57], v[42:43], 0, v[36:37]
	v_fmac_f32_e32 v52, v35, v13
	global_load_dwordx4 v[32:35], v[58:59], off
	global_load_dwordx4 v[36:39], v[56:57], off
	v_dot4c_i32_i8_e32 v61, v25, v53
	v_cvt_f32_i32_sdwa v53, sext(v27) dst_sel:DWORD dst_unused:UNUSED_PAD src0_sel:BYTE_1
	v_dot4c_i32_i8_e32 v61, v26, v54
	v_cvt_f32_i32_sdwa v54, sext(v24) dst_sel:DWORD dst_unused:UNUSED_PAD src0_sel:BYTE_2
	v_cvt_f32_i32_sdwa v60, sext(v25) dst_sel:DWORD dst_unused:UNUSED_PAD src0_sel:BYTE_2
	v_cvt_f32_i32_sdwa v62, sext(v26) dst_sel:DWORD dst_unused:UNUSED_PAD src0_sel:BYTE_2
	v_cvt_f32_i32_sdwa v63, sext(v27) dst_sel:DWORD dst_unused:UNUSED_PAD src0_sel:BYTE_2
	v_dot4c_i32_i8_e32 v61, v27, v55
	v_cvt_f32_i32_sdwa v55, sext(v24) dst_sel:DWORD dst_unused:UNUSED_PAD src0_sel:BYTE_3
	v_fmac_f32_e32 v52, v53, v5
	ds_bpermute_b32 v24, v44, v50 offset:128
	v_cvt_f32_i32_sdwa v65, sext(v26) dst_sel:DWORD dst_unused:UNUSED_PAD src0_sel:BYTE_3
	v_fmac_f32_e32 v52, v54, v2
	ds_bpermute_b32 v26, v44, v49 offset:128
	v_cvt_f32_i32_sdwa v64, sext(v25) dst_sel:DWORD dst_unused:UNUSED_PAD src0_sel:BYTE_3
	v_fmac_f32_e32 v52, v60, v10
	v_fmac_f32_e32 v52, v62, v14
	v_cvt_f32_i32_sdwa v66, sext(v27) dst_sel:DWORD dst_unused:UNUSED_PAD src0_sel:BYTE_3
	v_fmac_f32_e32 v52, v63, v6
	s_waitcnt lgkmcnt(1)
	v_ashrrev_i32_e32 v25, 31, v24
	v_fmac_f32_e32 v52, v55, v3
	v_lshlrev_b64 v[24:25], 7, v[24:25]
	s_waitcnt lgkmcnt(0)
	v_ashrrev_i32_e32 v27, 31, v26
	v_fmac_f32_e32 v52, v64, v11
	v_lshl_add_u64 v[56:57], v[42:43], 0, v[24:25]
	v_lshlrev_b64 v[24:25], 7, v[26:27]
	v_fmac_f32_e32 v52, v65, v15
	v_lshl_add_u64 v[58:59], v[42:43], 0, v[24:25]
	v_add_f32_dpp v25, v51, v51 quad_perm:[1,0,3,2] row_mask:0xf bank_mask:0xf bound_ctrl:1
	v_fmac_f32_e32 v52, v66, v7
	v_add_u32_dpp v24, v40, v40 quad_perm:[1,0,3,2] row_mask:0xf bank_mask:0xf bound_ctrl:1
	v_add_f32_dpp v25, v25, v25 quad_perm:[2,3,0,1] row_mask:0xf bank_mask:0xf bound_ctrl:1
	v_add_f32_dpp v27, v52, v52 quad_perm:[1,0,3,2] row_mask:0xf bank_mask:0xf bound_ctrl:1
	v_add_u32_dpp v24, v24, v24 quad_perm:[2,3,0,1] row_mask:0xf bank_mask:0xf bound_ctrl:1
	v_add_f32_dpp v25, v25, v25 row_half_mirror row_mask:0xf bank_mask:0xf bound_ctrl:1
	v_add_f32_dpp v27, v27, v27 quad_perm:[2,3,0,1] row_mask:0xf bank_mask:0xf bound_ctrl:1
	v_cndmask_b32_e32 v25, 0, v25, vcc
	v_add_u32_dpp v26, v61, v61 quad_perm:[1,0,3,2] row_mask:0xf bank_mask:0xf bound_ctrl:1
	v_add_f32_dpp v27, v27, v27 row_half_mirror row_mask:0xf bank_mask:0xf bound_ctrl:1
	v_add_u32_dpp v24, v24, v24 row_half_mirror row_mask:0xf bank_mask:0xf bound_ctrl:1
	v_add_u32_dpp v26, v26, v26 quad_perm:[2,3,0,1] row_mask:0xf bank_mask:0xf bound_ctrl:1
	v_cndmask_b32_e64 v40, v25, v27, s[0:1]
	s_waitcnt vmcnt(3)
	v_cvt_f32_i32_sdwa v25, sext(v16) dst_sel:DWORD dst_unused:UNUSED_PAD src0_sel:BYTE_0
	v_cndmask_b32_e32 v24, 0, v24, vcc
	v_add_u32_dpp v26, v26, v26 row_half_mirror row_mask:0xf bank_mask:0xf bound_ctrl:1
	v_cndmask_b32_e64 v51, v24, v26, s[0:1]
	v_cvt_f32_i32_sdwa v24, sext(v17) dst_sel:DWORD dst_unused:UNUSED_PAD src0_sel:BYTE_0
	v_cvt_f32_i32_sdwa v26, sext(v18) dst_sel:DWORD dst_unused:UNUSED_PAD src0_sel:BYTE_0
	v_fma_f32 v64, v25, v0, 0
	v_cvt_f32_i32_sdwa v25, sext(v19) dst_sel:DWORD dst_unused:UNUSED_PAD src0_sel:BYTE_0
	v_fmac_f32_e32 v64, v24, v8
	v_cvt_f32_i32_sdwa v24, sext(v16) dst_sel:DWORD dst_unused:UNUSED_PAD src0_sel:BYTE_1
	v_fmac_f32_e32 v64, v26, v12
	v_fmac_f32_e32 v64, v25, v4
	v_cvt_f32_i32_sdwa v25, sext(v17) dst_sel:DWORD dst_unused:UNUSED_PAD src0_sel:BYTE_1
	v_cvt_f32_i32_sdwa v26, sext(v18) dst_sel:DWORD dst_unused:UNUSED_PAD src0_sel:BYTE_1
	v_fmac_f32_e32 v64, v24, v1
	v_cvt_f32_i32_sdwa v24, sext(v19) dst_sel:DWORD dst_unused:UNUSED_PAD src0_sel:BYTE_1
	v_fmac_f32_e32 v64, v25, v9
	v_fmac_f32_e32 v64, v26, v13
	v_cvt_f32_i32_sdwa v25, sext(v16) dst_sel:DWORD dst_unused:UNUSED_PAD src0_sel:BYTE_2
	v_fmac_f32_e32 v64, v24, v5
	v_cvt_f32_i32_sdwa v24, sext(v17) dst_sel:DWORD dst_unused:UNUSED_PAD src0_sel:BYTE_2
	ds_bpermute_b32 v62, v44, v49 offset:160
	v_fmac_f32_e32 v64, v25, v2
	v_mov_b32_e32 v65, v41
	v_fmac_f32_e32 v64, v24, v10
	v_cvt_f32_i32_sdwa v24, sext(v18) dst_sel:DWORD dst_unused:UNUSED_PAD src0_sel:BYTE_2
	s_waitcnt vmcnt(2)
	v_dot4c_i32_i8_e32 v65, v16, v20
	v_cvt_f32_i32_sdwa v20, sext(v19) dst_sel:DWORD dst_unused:UNUSED_PAD src0_sel:BYTE_2
	ds_bpermute_b32 v60, v44, v50 offset:160
	v_fmac_f32_e32 v64, v24, v14
	global_load_dwordx4 v[24:27], v[56:57], off
	global_load_dwordx4 v[52:55], v[58:59], off
	v_dot4c_i32_i8_e32 v65, v17, v21
	v_cvt_f32_i32_sdwa v21, sext(v16) dst_sel:DWORD dst_unused:UNUSED_PAD src0_sel:BYTE_3
	v_dot4c_i32_i8_e32 v65, v18, v22
	v_cvt_f32_i32_sdwa v22, sext(v17) dst_sel:DWORD dst_unused:UNUSED_PAD src0_sel:BYTE_3
	v_dot4c_i32_i8_e32 v65, v19, v23
	v_cvt_f32_i32_sdwa v23, sext(v18) dst_sel:DWORD dst_unused:UNUSED_PAD src0_sel:BYTE_3
	v_cvt_f32_i32_sdwa v66, sext(v19) dst_sel:DWORD dst_unused:UNUSED_PAD src0_sel:BYTE_3
	s_waitcnt lgkmcnt(1)
	v_ashrrev_i32_e32 v63, 31, v62
	v_fmac_f32_e32 v64, v20, v6
	v_lshlrev_b64 v[18:19], 7, v[62:63]
	v_mov_b32_e32 v62, v41
	v_fmac_f32_e32 v64, v21, v3
	s_waitcnt lgkmcnt(0)
	v_ashrrev_i32_e32 v61, 31, v60
	s_waitcnt vmcnt(2)
	v_dot4c_i32_i8_e32 v62, v32, v36
	v_fmac_f32_e32 v64, v22, v11
	v_lshlrev_b64 v[16:17], 7, v[60:61]
	v_dot4c_i32_i8_e32 v62, v33, v37
	v_fmac_f32_e32 v64, v23, v15
	v_lshl_add_u64 v[16:17], v[42:43], 0, v[16:17]
	v_lshl_add_u64 v[18:19], v[42:43], 0, v[18:19]
	v_dot4c_i32_i8_e32 v62, v34, v38
	v_fmac_f32_e32 v64, v66, v7
	v_dot4c_i32_i8_e32 v62, v35, v39
	global_load_dwordx4 v[36:39], v[16:17], off
	global_load_dwordx4 v[56:59], v[18:19], off
	v_add_f32_dpp v18, v64, v64 quad_perm:[1,0,3,2] row_mask:0xf bank_mask:0xf bound_ctrl:1
	v_add_u32_dpp v17, v65, v65 quad_perm:[1,0,3,2] row_mask:0xf bank_mask:0xf bound_ctrl:1
	v_cvt_f32_i32_sdwa v19, sext(v34) dst_sel:DWORD dst_unused:UNUSED_PAD src0_sel:BYTE_0
	v_add_f32_dpp v18, v18, v18 quad_perm:[2,3,0,1] row_mask:0xf bank_mask:0xf bound_ctrl:1
	v_add_u32_dpp v17, v17, v17 quad_perm:[2,3,0,1] row_mask:0xf bank_mask:0xf bound_ctrl:1
	ds_bpermute_b32 v16, v44, v50 offset:192
	v_add_f32_dpp v18, v18, v18 row_half_mirror row_mask:0xf bank_mask:0xf bound_ctrl:1
	v_cndmask_b32_e64 v40, v40, v18, s[2:3]
	v_cvt_f32_i32_sdwa v18, sext(v32) dst_sel:DWORD dst_unused:UNUSED_PAD src0_sel:BYTE_0
	v_add_u32_dpp v17, v17, v17 row_half_mirror row_mask:0xf bank_mask:0xf bound_ctrl:1
	v_cndmask_b32_e64 v63, v51, v17, s[2:3]
	v_cvt_f32_i32_sdwa v17, sext(v33) dst_sel:DWORD dst_unused:UNUSED_PAD src0_sel:BYTE_0
	v_fma_f32 v51, v18, v0, 0
	v_cvt_f32_i32_sdwa v18, sext(v35) dst_sel:DWORD dst_unused:UNUSED_PAD src0_sel:BYTE_0
	v_cvt_f32_i32_sdwa v20, sext(v33) dst_sel:DWORD dst_unused:UNUSED_PAD src0_sel:BYTE_3
	v_fmac_f32_e32 v51, v17, v8
	v_cvt_f32_i32_sdwa v17, sext(v32) dst_sel:DWORD dst_unused:UNUSED_PAD src0_sel:BYTE_1
	v_fmac_f32_e32 v51, v19, v12
	v_fmac_f32_e32 v51, v18, v4
	v_cvt_f32_i32_sdwa v18, sext(v33) dst_sel:DWORD dst_unused:UNUSED_PAD src0_sel:BYTE_1
	v_cvt_f32_i32_sdwa v19, sext(v34) dst_sel:DWORD dst_unused:UNUSED_PAD src0_sel:BYTE_1
	v_fmac_f32_e32 v51, v17, v1
	v_cvt_f32_i32_sdwa v17, sext(v35) dst_sel:DWORD dst_unused:UNUSED_PAD src0_sel:BYTE_1
	v_fmac_f32_e32 v51, v18, v9
	v_fmac_f32_e32 v51, v19, v13
	v_cvt_f32_i32_sdwa v18, sext(v32) dst_sel:DWORD dst_unused:UNUSED_PAD src0_sel:BYTE_2
	v_fmac_f32_e32 v51, v17, v5
	v_cvt_f32_i32_sdwa v17, sext(v33) dst_sel:DWORD dst_unused:UNUSED_PAD src0_sel:BYTE_2
	v_cvt_f32_i32_sdwa v19, sext(v34) dst_sel:DWORD dst_unused:UNUSED_PAD src0_sel:BYTE_2
	v_fmac_f32_e32 v51, v18, v2
	v_cvt_f32_i32_sdwa v18, sext(v35) dst_sel:DWORD dst_unused:UNUSED_PAD src0_sel:BYTE_2
	v_fmac_f32_e32 v51, v17, v10
	v_fmac_f32_e32 v51, v19, v14
	v_cvt_f32_i32_sdwa v19, sext(v32) dst_sel:DWORD dst_unused:UNUSED_PAD src0_sel:BYTE_3
	v_fmac_f32_e32 v51, v18, v6
	ds_bpermute_b32 v18, v44, v49 offset:192
	s_waitcnt lgkmcnt(1)
	v_ashrrev_i32_e32 v17, 31, v16
	v_fmac_f32_e32 v51, v19, v3
	v_fmac_f32_e32 v51, v20, v11
	v_cvt_f32_i32_sdwa v20, sext(v34) dst_sel:DWORD dst_unused:UNUSED_PAD src0_sel:BYTE_3
	v_cvt_f32_i32_sdwa v34, sext(v35) dst_sel:DWORD dst_unused:UNUSED_PAD src0_sel:BYTE_3
	v_lshlrev_b64 v[16:17], 7, v[16:17]
	s_waitcnt lgkmcnt(0)
	v_ashrrev_i32_e32 v19, 31, v18
	v_lshl_add_u64 v[32:33], v[42:43], 0, v[16:17]
	v_lshlrev_b64 v[16:17], 7, v[18:19]
	v_lshl_add_u64 v[60:61], v[42:43], 0, v[16:17]
	v_fmac_f32_e32 v51, v20, v15
	global_load_dwordx4 v[16:19], v[32:33], off
	global_load_dwordx4 v[20:23], v[60:61], off
	ds_bpermute_b32 v32, v44, v50 offset:224
	v_fmac_f32_e32 v51, v34, v7
	ds_bpermute_b32 v34, v44, v49 offset:224
	v_mov_b32_e32 v60, v41
	v_add_f32_dpp v33, v51, v51 quad_perm:[1,0,3,2] row_mask:0xf bank_mask:0xf bound_ctrl:1
	s_waitcnt vmcnt(5)
	v_cvt_f32_i32_sdwa v35, sext(v26) dst_sel:DWORD dst_unused:UNUSED_PAD src0_sel:BYTE_0
	v_add_f32_dpp v33, v33, v33 quad_perm:[2,3,0,1] row_mask:0xf bank_mask:0xf bound_ctrl:1
	s_waitcnt vmcnt(4)
	v_dot4c_i32_i8_e32 v60, v24, v52
	v_dot4c_i32_i8_e32 v60, v25, v53
	v_add_f32_dpp v33, v33, v33 row_half_mirror row_mask:0xf bank_mask:0xf bound_ctrl:1
	v_cndmask_b32_e64 v40, v40, v33, s[4:5]
	s_waitcnt lgkmcnt(1)
	v_ashrrev_i32_e32 v33, 31, v32
	v_lshlrev_b64 v[32:33], 7, v[32:33]
	v_lshl_add_u64 v[50:51], v[42:43], 0, v[32:33]
	v_cvt_f32_i32_sdwa v33, sext(v25) dst_sel:DWORD dst_unused:UNUSED_PAD src0_sel:BYTE_0
	v_add_u32_dpp v32, v62, v62 quad_perm:[1,0,3,2] row_mask:0xf bank_mask:0xf bound_ctrl:1
	v_cvt_f32_i32_sdwa v52, sext(v27) dst_sel:DWORD dst_unused:UNUSED_PAD src0_sel:BYTE_0
	v_dot4c_i32_i8_e32 v60, v26, v54
	v_add_u32_dpp v32, v32, v32 quad_perm:[2,3,0,1] row_mask:0xf bank_mask:0xf bound_ctrl:1
	v_cvt_f32_i32_sdwa v53, sext(v24) dst_sel:DWORD dst_unused:UNUSED_PAD src0_sel:BYTE_2
	v_dot4c_i32_i8_e32 v60, v27, v55
	v_add_u32_dpp v32, v32, v32 row_half_mirror row_mask:0xf bank_mask:0xf bound_ctrl:1
	v_cndmask_b32_e64 v49, v63, v32, s[4:5]
	v_cvt_f32_i32_sdwa v32, sext(v24) dst_sel:DWORD dst_unused:UNUSED_PAD src0_sel:BYTE_0
	v_cvt_f32_i32_sdwa v55, sext(v25) dst_sel:DWORD dst_unused:UNUSED_PAD src0_sel:BYTE_2
	v_cvt_f32_i32_sdwa v61, sext(v26) dst_sel:DWORD dst_unused:UNUSED_PAD src0_sel:BYTE_3
	v_cvt_f32_i32_sdwa v62, sext(v27) dst_sel:DWORD dst_unused:UNUSED_PAD src0_sel:BYTE_3
	v_fma_f32 v54, v32, v0, 0
	v_fmac_f32_e32 v54, v33, v8
	v_cvt_f32_i32_sdwa v32, sext(v24) dst_sel:DWORD dst_unused:UNUSED_PAD src0_sel:BYTE_1
	v_fmac_f32_e32 v54, v35, v12
	v_cvt_f32_i32_sdwa v33, sext(v25) dst_sel:DWORD dst_unused:UNUSED_PAD src0_sel:BYTE_1
	v_fmac_f32_e32 v54, v52, v4
	v_cvt_f32_i32_sdwa v52, sext(v26) dst_sel:DWORD dst_unused:UNUSED_PAD src0_sel:BYTE_1
	v_fmac_f32_e32 v54, v32, v1
	v_fmac_f32_e32 v54, v33, v9
	s_waitcnt lgkmcnt(0)
	v_ashrrev_i32_e32 v35, 31, v34
	v_fmac_f32_e32 v54, v52, v13
	v_cvt_f32_i32_sdwa v52, sext(v27) dst_sel:DWORD dst_unused:UNUSED_PAD src0_sel:BYTE_1
	v_lshlrev_b64 v[32:33], 7, v[34:35]
	v_cvt_f32_i32_sdwa v34, sext(v26) dst_sel:DWORD dst_unused:UNUSED_PAD src0_sel:BYTE_2
	v_cvt_f32_i32_sdwa v35, sext(v27) dst_sel:DWORD dst_unused:UNUSED_PAD src0_sel:BYTE_2
	v_fmac_f32_e32 v54, v52, v5
	v_fmac_f32_e32 v54, v53, v2
	v_cvt_f32_i32_sdwa v24, sext(v24) dst_sel:DWORD dst_unused:UNUSED_PAD src0_sel:BYTE_3
	v_fmac_f32_e32 v54, v55, v10
	v_fmac_f32_e32 v54, v34, v14
	v_fmac_f32_e32 v54, v35, v6
	v_lshl_add_u64 v[52:53], v[42:43], 0, v[32:33]
	v_fmac_f32_e32 v54, v24, v3
	v_cvt_f32_i32_sdwa v55, sext(v25) dst_sel:DWORD dst_unused:UNUSED_PAD src0_sel:BYTE_3
	global_load_dwordx4 v[24:27], v[50:51], off
	global_load_dwordx4 v[32:35], v[52:53], off
	v_add_u32_dpp v50, v60, v60 quad_perm:[1,0,3,2] row_mask:0xf bank_mask:0xf bound_ctrl:1
	s_waitcnt vmcnt(5)
	v_cvt_f32_i32_sdwa v52, sext(v38) dst_sel:DWORD dst_unused:UNUSED_PAD src0_sel:BYTE_0
	v_fmac_f32_e32 v54, v55, v11
	v_fmac_f32_e32 v54, v61, v15
	v_fmac_f32_e32 v54, v62, v7
	v_add_u32_dpp v50, v50, v50 quad_perm:[2,3,0,1] row_mask:0xf bank_mask:0xf bound_ctrl:1
	v_cvt_f32_i32_sdwa v53, sext(v39) dst_sel:DWORD dst_unused:UNUSED_PAD src0_sel:BYTE_0
	v_add_f32_dpp v51, v54, v54 quad_perm:[1,0,3,2] row_mask:0xf bank_mask:0xf bound_ctrl:1
	v_add_u32_dpp v50, v50, v50 row_half_mirror row_mask:0xf bank_mask:0xf bound_ctrl:1
	v_cndmask_b32_e64 v49, v49, v50, s[6:7]
	v_add_f32_dpp v51, v51, v51 quad_perm:[2,3,0,1] row_mask:0xf bank_mask:0xf bound_ctrl:1
	v_cvt_f32_i32_sdwa v50, sext(v36) dst_sel:DWORD dst_unused:UNUSED_PAD src0_sel:BYTE_0
	v_mov_b32_e32 v54, v41
	v_add_f32_dpp v51, v51, v51 row_half_mirror row_mask:0xf bank_mask:0xf bound_ctrl:1
	v_cndmask_b32_e64 v40, v40, v51, s[6:7]
	v_cvt_f32_i32_sdwa v51, sext(v37) dst_sel:DWORD dst_unused:UNUSED_PAD src0_sel:BYTE_0
	v_fma_f32 v50, v50, v0, 0
	s_waitcnt vmcnt(4)
	v_dot4c_i32_i8_e32 v54, v36, v56
	v_dot4c_i32_i8_e32 v54, v37, v57
	v_fmac_f32_e32 v50, v51, v8
	v_cvt_f32_i32_sdwa v51, sext(v36) dst_sel:DWORD dst_unused:UNUSED_PAD src0_sel:BYTE_1
	v_fmac_f32_e32 v50, v52, v12
	v_cvt_f32_i32_sdwa v52, sext(v37) dst_sel:DWORD dst_unused:UNUSED_PAD src0_sel:BYTE_1
	v_fmac_f32_e32 v50, v53, v4
	v_cvt_f32_i32_sdwa v53, sext(v38) dst_sel:DWORD dst_unused:UNUSED_PAD src0_sel:BYTE_1
	v_fmac_f32_e32 v50, v51, v1
	v_cvt_f32_i32_sdwa v51, sext(v39) dst_sel:DWORD dst_unused:UNUSED_PAD src0_sel:BYTE_1
	v_fmac_f32_e32 v50, v52, v9
	v_cvt_f32_i32_sdwa v52, sext(v36) dst_sel:DWORD dst_unused:UNUSED_PAD src0_sel:BYTE_2
	v_fmac_f32_e32 v50, v53, v13
	v_cvt_f32_i32_sdwa v53, sext(v37) dst_sel:DWORD dst_unused:UNUSED_PAD src0_sel:BYTE_2
	v_fmac_f32_e32 v50, v51, v5
	v_cvt_f32_i32_sdwa v51, sext(v38) dst_sel:DWORD dst_unused:UNUSED_PAD src0_sel:BYTE_2
	v_fmac_f32_e32 v50, v52, v2
	v_cvt_f32_i32_sdwa v52, sext(v39) dst_sel:DWORD dst_unused:UNUSED_PAD src0_sel:BYTE_2
	v_cvt_f32_i32_sdwa v36, sext(v36) dst_sel:DWORD dst_unused:UNUSED_PAD src0_sel:BYTE_3
	v_fmac_f32_e32 v50, v53, v10
	v_fmac_f32_e32 v50, v51, v14
	v_fmac_f32_e32 v50, v52, v6
	v_fmac_f32_e32 v50, v36, v3
	v_cvt_f32_i32_sdwa v36, sext(v37) dst_sel:DWORD dst_unused:UNUSED_PAD src0_sel:BYTE_3
	v_cvt_f32_i32_sdwa v37, sext(v38) dst_sel:DWORD dst_unused:UNUSED_PAD src0_sel:BYTE_3
	v_dot4c_i32_i8_e32 v54, v38, v58
	v_mov_b32_e32 v38, v41
	v_cvt_f32_i32_sdwa v51, sext(v39) dst_sel:DWORD dst_unused:UNUSED_PAD src0_sel:BYTE_3
	s_waitcnt vmcnt(2)
	v_dot4c_i32_i8_e32 v38, v16, v20
	v_cvt_f32_i32_sdwa v20, sext(v16) dst_sel:DWORD dst_unused:UNUSED_PAD src0_sel:BYTE_0
	v_dot4c_i32_i8_e32 v38, v17, v21
	v_cvt_f32_i32_sdwa v21, sext(v17) dst_sel:DWORD dst_unused:UNUSED_PAD src0_sel:BYTE_0
	v_fmac_f32_e32 v50, v36, v11
	v_dot4c_i32_i8_e32 v38, v18, v22
	v_cvt_f32_i32_sdwa v22, sext(v18) dst_sel:DWORD dst_unused:UNUSED_PAD src0_sel:BYTE_0
	v_fmac_f32_e32 v50, v37, v15
	v_dot4c_i32_i8_e32 v54, v39, v59
	v_cvt_f32_i32_sdwa v39, sext(v19) dst_sel:DWORD dst_unused:UNUSED_PAD src0_sel:BYTE_0
	v_fmac_f32_e32 v50, v51, v7
	v_fma_f32 v20, v20, v0, 0
	v_fmac_f32_e32 v20, v21, v8
	v_add_f32_dpp v37, v50, v50 quad_perm:[1,0,3,2] row_mask:0xf bank_mask:0xf bound_ctrl:1
	v_cvt_f32_i32_sdwa v21, sext(v16) dst_sel:DWORD dst_unused:UNUSED_PAD src0_sel:BYTE_1
	v_fmac_f32_e32 v20, v22, v12
	v_add_f32_dpp v37, v37, v37 quad_perm:[2,3,0,1] row_mask:0xf bank_mask:0xf bound_ctrl:1
	v_cvt_f32_i32_sdwa v22, sext(v17) dst_sel:DWORD dst_unused:UNUSED_PAD src0_sel:BYTE_1
	v_fmac_f32_e32 v20, v39, v4
	v_add_f32_dpp v37, v37, v37 row_half_mirror row_mask:0xf bank_mask:0xf bound_ctrl:1
	v_cvt_f32_i32_sdwa v39, sext(v18) dst_sel:DWORD dst_unused:UNUSED_PAD src0_sel:BYTE_1
	v_cndmask_b32_e64 v37, v40, v37, s[8:9]
	v_cvt_f32_i32_sdwa v40, sext(v19) dst_sel:DWORD dst_unused:UNUSED_PAD src0_sel:BYTE_1
	v_fmac_f32_e32 v20, v21, v1
	v_cvt_f32_i32_sdwa v21, sext(v16) dst_sel:DWORD dst_unused:UNUSED_PAD src0_sel:BYTE_2
	v_fmac_f32_e32 v20, v22, v9
	v_cvt_f32_i32_sdwa v22, sext(v17) dst_sel:DWORD dst_unused:UNUSED_PAD src0_sel:BYTE_2
	v_fmac_f32_e32 v20, v39, v13
	v_cvt_f32_i32_sdwa v39, sext(v18) dst_sel:DWORD dst_unused:UNUSED_PAD src0_sel:BYTE_2
	v_fmac_f32_e32 v20, v40, v5
	v_cvt_f32_i32_sdwa v40, sext(v19) dst_sel:DWORD dst_unused:UNUSED_PAD src0_sel:BYTE_2
	v_fmac_f32_e32 v20, v21, v2
	v_cvt_f32_i32_sdwa v16, sext(v16) dst_sel:DWORD dst_unused:UNUSED_PAD src0_sel:BYTE_3
	v_fmac_f32_e32 v20, v22, v10
	v_cvt_f32_i32_sdwa v17, sext(v17) dst_sel:DWORD dst_unused:UNUSED_PAD src0_sel:BYTE_3
	v_fmac_f32_e32 v20, v39, v14
	v_cvt_f32_i32_sdwa v18, sext(v18) dst_sel:DWORD dst_unused:UNUSED_PAD src0_sel:BYTE_3
	v_fmac_f32_e32 v20, v40, v6
	v_cvt_f32_i32_sdwa v21, sext(v19) dst_sel:DWORD dst_unused:UNUSED_PAD src0_sel:BYTE_3
	v_fmac_f32_e32 v20, v16, v3
	v_fmac_f32_e32 v20, v17, v11
	v_fmac_f32_e32 v20, v18, v15
	v_fmac_f32_e32 v20, v21, v7
	v_dot4c_i32_i8_e32 v38, v19, v23
	s_waitcnt vmcnt(1)
	v_cvt_f32_i32_sdwa v19, sext(v24) dst_sel:DWORD dst_unused:UNUSED_PAD src0_sel:BYTE_0
	v_add_f32_dpp v17, v20, v20 quad_perm:[1,0,3,2] row_mask:0xf bank_mask:0xf bound_ctrl:1
	v_cvt_f32_i32_sdwa v20, sext(v25) dst_sel:DWORD dst_unused:UNUSED_PAD src0_sel:BYTE_0
	v_cvt_f32_i32_sdwa v21, sext(v26) dst_sel:DWORD dst_unused:UNUSED_PAD src0_sel:BYTE_0
	v_cvt_f32_i32_sdwa v22, sext(v27) dst_sel:DWORD dst_unused:UNUSED_PAD src0_sel:BYTE_0
	v_fma_f32 v19, v19, v0, 0
	v_fmac_f32_e32 v19, v20, v8
	v_cvt_f32_i32_sdwa v20, sext(v24) dst_sel:DWORD dst_unused:UNUSED_PAD src0_sel:BYTE_1
	v_fmac_f32_e32 v19, v21, v12
	v_cvt_f32_i32_sdwa v21, sext(v25) dst_sel:DWORD dst_unused:UNUSED_PAD src0_sel:BYTE_1
	v_fmac_f32_e32 v19, v22, v4
	v_cvt_f32_i32_sdwa v22, sext(v26) dst_sel:DWORD dst_unused:UNUSED_PAD src0_sel:BYTE_1
	v_cvt_f32_i32_sdwa v23, sext(v27) dst_sel:DWORD dst_unused:UNUSED_PAD src0_sel:BYTE_1
	v_add_u32_dpp v36, v54, v54 quad_perm:[1,0,3,2] row_mask:0xf bank_mask:0xf bound_ctrl:1
	v_fmac_f32_e32 v19, v20, v1
	v_cvt_f32_i32_sdwa v20, sext(v24) dst_sel:DWORD dst_unused:UNUSED_PAD src0_sel:BYTE_2
	v_add_u32_dpp v36, v36, v36 quad_perm:[2,3,0,1] row_mask:0xf bank_mask:0xf bound_ctrl:1
	v_add_u32_dpp v16, v38, v38 quad_perm:[1,0,3,2] row_mask:0xf bank_mask:0xf bound_ctrl:1
	v_fmac_f32_e32 v19, v21, v9
	v_cvt_f32_i32_sdwa v21, sext(v25) dst_sel:DWORD dst_unused:UNUSED_PAD src0_sel:BYTE_2
	v_add_u32_dpp v36, v36, v36 row_half_mirror row_mask:0xf bank_mask:0xf bound_ctrl:1
	v_add_u32_dpp v16, v16, v16 quad_perm:[2,3,0,1] row_mask:0xf bank_mask:0xf bound_ctrl:1
	v_fmac_f32_e32 v19, v22, v13
	v_cvt_f32_i32_sdwa v22, sext(v26) dst_sel:DWORD dst_unused:UNUSED_PAD src0_sel:BYTE_2
	v_cndmask_b32_e64 v36, v49, v36, s[8:9]
	v_add_u32_dpp v16, v16, v16 row_half_mirror row_mask:0xf bank_mask:0xf bound_ctrl:1
	v_fmac_f32_e32 v19, v23, v5
	v_cvt_f32_i32_sdwa v23, sext(v27) dst_sel:DWORD dst_unused:UNUSED_PAD src0_sel:BYTE_2
	v_cndmask_b32_e64 v18, v36, v16, s[10:11]
	v_mov_b32_e32 v16, v41
	v_fmac_f32_e32 v19, v20, v2
	v_cvt_f32_i32_sdwa v20, sext(v24) dst_sel:DWORD dst_unused:UNUSED_PAD src0_sel:BYTE_3
	s_waitcnt vmcnt(0)
	v_dot4c_i32_i8_e32 v16, v24, v32
	v_fmac_f32_e32 v19, v21, v10
	v_cvt_f32_i32_sdwa v21, sext(v25) dst_sel:DWORD dst_unused:UNUSED_PAD src0_sel:BYTE_3
	v_dot4c_i32_i8_e32 v16, v25, v33
	v_fmac_f32_e32 v19, v22, v14
	v_cvt_f32_i32_sdwa v22, sext(v26) dst_sel:DWORD dst_unused:UNUSED_PAD src0_sel:BYTE_3
	v_dot4c_i32_i8_e32 v16, v26, v34
	v_fmac_f32_e32 v19, v23, v6
	v_cvt_f32_i32_sdwa v23, sext(v27) dst_sel:DWORD dst_unused:UNUSED_PAD src0_sel:BYTE_3
	v_fmac_f32_e32 v19, v20, v3
	v_dot4c_i32_i8_e32 v16, v27, v35
	v_fmac_f32_e32 v19, v21, v11
	v_fmac_f32_e32 v19, v22, v15
	v_fmac_f32_e32 v19, v23, v7
	v_add_u32_dpp v16, v16, v16 quad_perm:[1,0,3,2] row_mask:0xf bank_mask:0xf bound_ctrl:1
	v_add_f32_dpp v17, v17, v17 quad_perm:[2,3,0,1] row_mask:0xf bank_mask:0xf bound_ctrl:1
	v_add_f32_dpp v19, v19, v19 quad_perm:[1,0,3,2] row_mask:0xf bank_mask:0xf bound_ctrl:1
	v_add_u32_dpp v16, v16, v16 quad_perm:[2,3,0,1] row_mask:0xf bank_mask:0xf bound_ctrl:1
	v_add_f32_dpp v17, v17, v17 row_half_mirror row_mask:0xf bank_mask:0xf bound_ctrl:1
	v_add_f32_dpp v19, v19, v19 quad_perm:[2,3,0,1] row_mask:0xf bank_mask:0xf bound_ctrl:1
	v_add_u32_dpp v20, v16, v16 row_half_mirror row_mask:0xf bank_mask:0xf bound_ctrl:1
	ds_bpermute_b32 v16, v44, v48
	v_cndmask_b32_e64 v17, v37, v17, s[10:11]
	v_add_f32_dpp v19, v19, v19 row_half_mirror row_mask:0xf bank_mask:0xf bound_ctrl:1
	v_cndmask_b32_e64 v17, v17, v19, s[12:13]
	v_cndmask_b32_e64 v18, v18, v20, s[12:13]
	global_store_dword v[28:29], v18, off offset:256
	global_store_dword v[30:31], v17, off offset:256
	s_waitcnt lgkmcnt(0)
	v_ashrrev_i32_e32 v17, 31, v16
	v_lshlrev_b64 v[16:17], 7, v[16:17]
	v_lshl_add_u64 v[16:17], v[42:43], 0, v[16:17]
	global_load_dwordx4 v[24:27], v[16:17], off
	ds_bpermute_b32 v16, v44, v47
	ds_bpermute_b32 v18, v44, v48 offset:32
	ds_bpermute_b32 v20, v44, v47 offset:32
	s_waitcnt lgkmcnt(2)
	v_ashrrev_i32_e32 v17, 31, v16
	v_lshlrev_b64 v[16:17], 7, v[16:17]
	v_lshl_add_u64 v[16:17], v[42:43], 0, v[16:17]
	s_waitcnt lgkmcnt(1)
	v_ashrrev_i32_e32 v19, 31, v18
	global_load_dwordx4 v[32:35], v[16:17], off
	v_lshlrev_b64 v[16:17], 7, v[18:19]
	s_waitcnt lgkmcnt(0)
	v_ashrrev_i32_e32 v21, 31, v20
	v_lshl_add_u64 v[16:17], v[42:43], 0, v[16:17]
	v_lshlrev_b64 v[18:19], 7, v[20:21]
	v_lshl_add_u64 v[18:19], v[42:43], 0, v[18:19]
	global_load_dwordx4 v[36:39], v[16:17], off
	global_load_dwordx4 v[50:53], v[18:19], off
	ds_bpermute_b32 v16, v44, v48 offset:64
	ds_bpermute_b32 v18, v44, v47 offset:64
	s_waitcnt lgkmcnt(1)
	v_ashrrev_i32_e32 v17, 31, v16
	v_lshlrev_b64 v[16:17], 7, v[16:17]
	s_waitcnt lgkmcnt(0)
	v_ashrrev_i32_e32 v19, 31, v18
	v_lshl_add_u64 v[54:55], v[42:43], 0, v[16:17]
	v_lshlrev_b64 v[16:17], 7, v[18:19]
	v_lshl_add_u64 v[56:57], v[42:43], 0, v[16:17]
	global_load_dwordx4 v[16:19], v[54:55], off
	global_load_dwordx4 v[20:23], v[56:57], off
	ds_bpermute_b32 v54, v44, v48 offset:96
	ds_bpermute_b32 v56, v44, v47 offset:96
	s_waitcnt vmcnt(5)
	v_cvt_f32_i32_sdwa v40, sext(v24) dst_sel:DWORD dst_unused:UNUSED_PAD src0_sel:BYTE_0
	v_cvt_f32_i32_sdwa v49, sext(v25) dst_sel:DWORD dst_unused:UNUSED_PAD src0_sel:BYTE_0
	v_cvt_f32_i32_sdwa v55, sext(v26) dst_sel:DWORD dst_unused:UNUSED_PAD src0_sel:BYTE_0
	v_cvt_f32_i32_sdwa v57, sext(v24) dst_sel:DWORD dst_unused:UNUSED_PAD src0_sel:BYTE_1
	v_fma_f32 v40, v40, v0, 0
	v_fmac_f32_e32 v40, v49, v8
	v_cvt_f32_i32_sdwa v49, sext(v27) dst_sel:DWORD dst_unused:UNUSED_PAD src0_sel:BYTE_0
	v_fmac_f32_e32 v40, v55, v12
	v_cvt_f32_i32_sdwa v58, sext(v26) dst_sel:DWORD dst_unused:UNUSED_PAD src0_sel:BYTE_2
	s_waitcnt lgkmcnt(1)
	v_ashrrev_i32_e32 v55, 31, v54
	v_fmac_f32_e32 v40, v49, v4
	v_cvt_f32_i32_sdwa v49, sext(v25) dst_sel:DWORD dst_unused:UNUSED_PAD src0_sel:BYTE_1
	v_fmac_f32_e32 v40, v57, v1
	v_cvt_f32_i32_sdwa v57, sext(v26) dst_sel:DWORD dst_unused:UNUSED_PAD src0_sel:BYTE_1
	v_lshlrev_b64 v[54:55], 7, v[54:55]
	v_fmac_f32_e32 v40, v49, v9
	v_cvt_f32_i32_sdwa v49, sext(v27) dst_sel:DWORD dst_unused:UNUSED_PAD src0_sel:BYTE_1
	v_fmac_f32_e32 v40, v57, v13
	v_cvt_f32_i32_sdwa v57, sext(v24) dst_sel:DWORD dst_unused:UNUSED_PAD src0_sel:BYTE_2
	v_lshl_add_u64 v[54:55], v[42:43], 0, v[54:55]
	v_fmac_f32_e32 v40, v49, v5
	v_cvt_f32_i32_sdwa v49, sext(v25) dst_sel:DWORD dst_unused:UNUSED_PAD src0_sel:BYTE_2
	v_fmac_f32_e32 v40, v57, v2
	s_waitcnt lgkmcnt(0)
	v_ashrrev_i32_e32 v57, 31, v56
	v_lshlrev_b64 v[56:57], 7, v[56:57]
	v_fmac_f32_e32 v40, v49, v10
	v_cvt_f32_i32_sdwa v49, sext(v27) dst_sel:DWORD dst_unused:UNUSED_PAD src0_sel:BYTE_2
	v_fmac_f32_e32 v40, v58, v14
	v_cvt_f32_i32_sdwa v58, sext(v24) dst_sel:DWORD dst_unused:UNUSED_PAD src0_sel:BYTE_3
	v_lshl_add_u64 v[56:57], v[42:43], 0, v[56:57]
	v_fmac_f32_e32 v40, v49, v6
	v_cvt_f32_i32_sdwa v49, sext(v25) dst_sel:DWORD dst_unused:UNUSED_PAD src0_sel:BYTE_3
	v_fmac_f32_e32 v40, v58, v3
	v_cvt_f32_i32_sdwa v58, sext(v26) dst_sel:DWORD dst_unused:UNUSED_PAD src0_sel:BYTE_3
	s_waitcnt vmcnt(3)
	v_cvt_f32_i32_sdwa v59, sext(v39) dst_sel:DWORD dst_unused:UNUSED_PAD src0_sel:BYTE_1
	v_fmac_f32_e32 v40, v49, v11
	v_mov_b32_e32 v49, v41
	v_fmac_f32_e32 v40, v58, v15
	v_cvt_f32_i32_sdwa v58, sext(v27) dst_sel:DWORD dst_unused:UNUSED_PAD src0_sel:BYTE_3
	v_dot4c_i32_i8_e32 v49, v24, v32
	v_cvt_f32_i32_sdwa v24, sext(v36) dst_sel:DWORD dst_unused:UNUSED_PAD src0_sel:BYTE_0
	v_dot4c_i32_i8_e32 v49, v25, v33
	v_fmac_f32_e32 v40, v58, v7
	v_mov_b32_e32 v58, v41
	s_waitcnt vmcnt(2)
	v_dot4c_i32_i8_e32 v58, v36, v50
	v_dot4c_i32_i8_e32 v58, v37, v51
	v_fma_f32 v51, v24, v0, 0
	v_cvt_f32_i32_sdwa v24, sext(v37) dst_sel:DWORD dst_unused:UNUSED_PAD src0_sel:BYTE_0
	v_cvt_f32_i32_sdwa v25, sext(v38) dst_sel:DWORD dst_unused:UNUSED_PAD src0_sel:BYTE_0
	v_dot4c_i32_i8_e32 v49, v26, v34
	v_cvt_f32_i32_sdwa v26, sext(v39) dst_sel:DWORD dst_unused:UNUSED_PAD src0_sel:BYTE_0
	v_dot4c_i32_i8_e32 v49, v27, v35
	v_cvt_f32_i32_sdwa v27, sext(v36) dst_sel:DWORD dst_unused:UNUSED_PAD src0_sel:BYTE_1
	v_fmac_f32_e32 v51, v24, v8
	v_fmac_f32_e32 v51, v25, v12
	v_fmac_f32_e32 v51, v26, v4
	v_fmac_f32_e32 v51, v27, v1
	global_load_dwordx4 v[24:27], v[54:55], off
	global_load_dwordx4 v[32:35], v[56:57], off
	v_cvt_f32_i32_sdwa v50, sext(v37) dst_sel:DWORD dst_unused:UNUSED_PAD src0_sel:BYTE_1
	v_dot4c_i32_i8_e32 v58, v38, v52
	v_cvt_f32_i32_sdwa v52, sext(v38) dst_sel:DWORD dst_unused:UNUSED_PAD src0_sel:BYTE_1
	v_cvt_f32_i32_sdwa v60, sext(v36) dst_sel:DWORD dst_unused:UNUSED_PAD src0_sel:BYTE_2
	v_cvt_f32_i32_sdwa v61, sext(v37) dst_sel:DWORD dst_unused:UNUSED_PAD src0_sel:BYTE_2
	v_fmac_f32_e32 v51, v50, v9
	v_cvt_f32_i32_sdwa v62, sext(v38) dst_sel:DWORD dst_unused:UNUSED_PAD src0_sel:BYTE_2
	v_fmac_f32_e32 v51, v52, v13
	v_cvt_f32_i32_sdwa v63, sext(v39) dst_sel:DWORD dst_unused:UNUSED_PAD src0_sel:BYTE_2
	v_fmac_f32_e32 v51, v59, v5
	v_dot4c_i32_i8_e32 v58, v39, v53
	v_cvt_f32_i32_sdwa v53, sext(v36) dst_sel:DWORD dst_unused:UNUSED_PAD src0_sel:BYTE_3
	v_fmac_f32_e32 v51, v60, v2
	v_cvt_f32_i32_sdwa v64, sext(v37) dst_sel:DWORD dst_unused:UNUSED_PAD src0_sel:BYTE_3
	v_fmac_f32_e32 v51, v61, v10
	v_cvt_f32_i32_sdwa v65, sext(v38) dst_sel:DWORD dst_unused:UNUSED_PAD src0_sel:BYTE_3
	v_fmac_f32_e32 v51, v62, v14
	v_cvt_f32_i32_sdwa v66, sext(v39) dst_sel:DWORD dst_unused:UNUSED_PAD src0_sel:BYTE_3
	v_fmac_f32_e32 v51, v63, v6
	v_fmac_f32_e32 v51, v53, v3
	v_fmac_f32_e32 v51, v64, v11
	v_fmac_f32_e32 v51, v65, v15
	v_add_f32_dpp v40, v40, v40 quad_perm:[1,0,3,2] row_mask:0xf bank_mask:0xf bound_ctrl:1
	v_fmac_f32_e32 v51, v66, v7
	v_add_u32_dpp v49, v49, v49 quad_perm:[1,0,3,2] row_mask:0xf bank_mask:0xf bound_ctrl:1
	v_add_f32_dpp v40, v40, v40 quad_perm:[2,3,0,1] row_mask:0xf bank_mask:0xf bound_ctrl:1
	v_add_f32_dpp v51, v51, v51 quad_perm:[1,0,3,2] row_mask:0xf bank_mask:0xf bound_ctrl:1
	v_add_u32_dpp v49, v49, v49 quad_perm:[2,3,0,1] row_mask:0xf bank_mask:0xf bound_ctrl:1
	v_add_f32_dpp v40, v40, v40 row_half_mirror row_mask:0xf bank_mask:0xf bound_ctrl:1
	v_add_u32_dpp v53, v58, v58 quad_perm:[1,0,3,2] row_mask:0xf bank_mask:0xf bound_ctrl:1
	v_add_f32_dpp v51, v51, v51 quad_perm:[2,3,0,1] row_mask:0xf bank_mask:0xf bound_ctrl:1
	v_add_u32_dpp v49, v49, v49 row_half_mirror row_mask:0xf bank_mask:0xf bound_ctrl:1
	v_cndmask_b32_e32 v40, 0, v40, vcc
	v_add_u32_dpp v53, v53, v53 quad_perm:[2,3,0,1] row_mask:0xf bank_mask:0xf bound_ctrl:1
	v_add_f32_dpp v51, v51, v51 row_half_mirror row_mask:0xf bank_mask:0xf bound_ctrl:1
	v_cndmask_b32_e32 v49, 0, v49, vcc
	v_add_u32_dpp v53, v53, v53 row_half_mirror row_mask:0xf bank_mask:0xf bound_ctrl:1
	v_cndmask_b32_e64 v40, v40, v51, s[0:1]
	s_waitcnt vmcnt(3)
	v_cvt_f32_i32_sdwa v51, sext(v16) dst_sel:DWORD dst_unused:UNUSED_PAD src0_sel:BYTE_0
	v_cndmask_b32_e64 v49, v49, v53, s[0:1]
	v_cvt_f32_i32_sdwa v53, sext(v17) dst_sel:DWORD dst_unused:UNUSED_PAD src0_sel:BYTE_0
	v_mov_b32_e32 v58, v41
	v_cvt_f32_i32_sdwa v54, sext(v18) dst_sel:DWORD dst_unused:UNUSED_PAD src0_sel:BYTE_0
	s_waitcnt vmcnt(2)
	v_dot4c_i32_i8_e32 v58, v16, v20
	v_cvt_f32_i32_sdwa v20, sext(v19) dst_sel:DWORD dst_unused:UNUSED_PAD src0_sel:BYTE_0
	ds_bpermute_b32 v36, v44, v48 offset:128
	v_fma_f32 v59, v51, v0, 0
	ds_bpermute_b32 v38, v44, v47 offset:128
	v_fmac_f32_e32 v59, v53, v8
	v_cvt_f32_i32_sdwa v51, sext(v16) dst_sel:DWORD dst_unused:UNUSED_PAD src0_sel:BYTE_1
	v_fmac_f32_e32 v59, v54, v12
	v_cvt_f32_i32_sdwa v53, sext(v17) dst_sel:DWORD dst_unused:UNUSED_PAD src0_sel:BYTE_1
	v_fmac_f32_e32 v59, v20, v4
	v_cvt_f32_i32_sdwa v20, sext(v18) dst_sel:DWORD dst_unused:UNUSED_PAD src0_sel:BYTE_1
	v_dot4c_i32_i8_e32 v58, v17, v21
	v_cvt_f32_i32_sdwa v21, sext(v19) dst_sel:DWORD dst_unused:UNUSED_PAD src0_sel:BYTE_1
	s_waitcnt lgkmcnt(1)
	v_ashrrev_i32_e32 v37, 31, v36
	v_fmac_f32_e32 v59, v51, v1
	v_lshlrev_b64 v[36:37], 7, v[36:37]
	s_waitcnt lgkmcnt(0)
	v_ashrrev_i32_e32 v39, 31, v38
	v_fmac_f32_e32 v59, v53, v9
	v_lshl_add_u64 v[36:37], v[42:43], 0, v[36:37]
	v_lshlrev_b64 v[38:39], 7, v[38:39]
	v_dot4c_i32_i8_e32 v58, v18, v22
	v_fmac_f32_e32 v59, v20, v13
	v_lshl_add_u64 v[38:39], v[42:43], 0, v[38:39]
	v_cvt_f32_i32_sdwa v51, sext(v16) dst_sel:DWORD dst_unused:UNUSED_PAD src0_sel:BYTE_2
	v_fmac_f32_e32 v59, v21, v5
	v_cvt_f32_i32_sdwa v54, sext(v17) dst_sel:DWORD dst_unused:UNUSED_PAD src0_sel:BYTE_2
	v_cvt_f32_i32_sdwa v55, sext(v18) dst_sel:DWORD dst_unused:UNUSED_PAD src0_sel:BYTE_2
	v_cvt_f32_i32_sdwa v56, sext(v19) dst_sel:DWORD dst_unused:UNUSED_PAD src0_sel:BYTE_2
	v_dot4c_i32_i8_e32 v58, v19, v23
	v_cvt_f32_i32_sdwa v57, sext(v16) dst_sel:DWORD dst_unused:UNUSED_PAD src0_sel:BYTE_3
	v_cvt_f32_i32_sdwa v60, sext(v17) dst_sel:DWORD dst_unused:UNUSED_PAD src0_sel:BYTE_3
	v_cvt_f32_i32_sdwa v61, sext(v18) dst_sel:DWORD dst_unused:UNUSED_PAD src0_sel:BYTE_3
	v_cvt_f32_i32_sdwa v62, sext(v19) dst_sel:DWORD dst_unused:UNUSED_PAD src0_sel:BYTE_3
	global_load_dwordx4 v[16:19], v[36:37], off
	global_load_dwordx4 v[20:23], v[38:39], off
	v_fmac_f32_e32 v59, v51, v2
	ds_bpermute_b32 v50, v44, v48 offset:160
	v_fmac_f32_e32 v59, v54, v10
	ds_bpermute_b32 v52, v44, v47 offset:160
	v_fmac_f32_e32 v59, v55, v14
	ds_bpermute_b32 v54, v44, v48 offset:192
	v_fmac_f32_e32 v59, v56, v6
	v_fmac_f32_e32 v59, v57, v3
	ds_bpermute_b32 v56, v44, v47 offset:192
	v_fmac_f32_e32 v59, v60, v11
	v_mov_b32_e32 v60, v41
	s_waitcnt lgkmcnt(3)
	v_ashrrev_i32_e32 v51, 31, v50
	s_waitcnt vmcnt(2)
	v_dot4c_i32_i8_e32 v60, v24, v32
	v_lshlrev_b64 v[36:37], 7, v[50:51]
	s_waitcnt lgkmcnt(2)
	v_ashrrev_i32_e32 v53, 31, v52
	v_dot4c_i32_i8_e32 v60, v25, v33
	v_lshl_add_u64 v[50:51], v[42:43], 0, v[36:37]
	v_lshlrev_b64 v[36:37], 7, v[52:53]
	v_dot4c_i32_i8_e32 v60, v26, v34
	s_waitcnt lgkmcnt(1)
	v_ashrrev_i32_e32 v55, 31, v54
	v_lshl_add_u64 v[52:53], v[42:43], 0, v[36:37]
	v_dot4c_i32_i8_e32 v60, v27, v35
	global_load_dwordx4 v[32:35], v[50:51], off
	global_load_dwordx4 v[36:39], v[52:53], off
	v_lshlrev_b64 v[50:51], 7, v[54:55]
	s_waitcnt lgkmcnt(0)
	v_ashrrev_i32_e32 v57, 31, v56
	v_fmac_f32_e32 v59, v61, v15
	v_lshl_add_u64 v[52:53], v[42:43], 0, v[50:51]
	v_lshlrev_b64 v[50:51], 7, v[56:57]
	v_fmac_f32_e32 v59, v62, v7
	v_lshl_add_u64 v[54:55], v[42:43], 0, v[50:51]
	v_add_u32_dpp v50, v58, v58 quad_perm:[1,0,3,2] row_mask:0xf bank_mask:0xf bound_ctrl:1
	v_add_f32_dpp v51, v59, v59 quad_perm:[1,0,3,2] row_mask:0xf bank_mask:0xf bound_ctrl:1
	v_cvt_f32_i32_sdwa v56, sext(v25) dst_sel:DWORD dst_unused:UNUSED_PAD src0_sel:BYTE_0
	v_add_u32_dpp v50, v50, v50 quad_perm:[2,3,0,1] row_mask:0xf bank_mask:0xf bound_ctrl:1
	v_add_f32_dpp v51, v51, v51 quad_perm:[2,3,0,1] row_mask:0xf bank_mask:0xf bound_ctrl:1
	v_cvt_f32_i32_sdwa v57, sext(v26) dst_sel:DWORD dst_unused:UNUSED_PAD src0_sel:BYTE_3
	v_add_u32_dpp v50, v50, v50 row_half_mirror row_mask:0xf bank_mask:0xf bound_ctrl:1
	v_add_f32_dpp v51, v51, v51 row_half_mirror row_mask:0xf bank_mask:0xf bound_ctrl:1
	v_cndmask_b32_e64 v40, v40, v51, s[2:3]
	v_cvt_f32_i32_sdwa v51, sext(v24) dst_sel:DWORD dst_unused:UNUSED_PAD src0_sel:BYTE_0
	v_cndmask_b32_e64 v58, v49, v50, s[2:3]
	v_cvt_f32_i32_sdwa v49, sext(v26) dst_sel:DWORD dst_unused:UNUSED_PAD src0_sel:BYTE_0
	v_cvt_f32_i32_sdwa v50, sext(v27) dst_sel:DWORD dst_unused:UNUSED_PAD src0_sel:BYTE_0
	v_fma_f32 v59, v51, v0, 0
	v_fmac_f32_e32 v59, v56, v8
	v_fmac_f32_e32 v59, v49, v12
	v_cvt_f32_i32_sdwa v49, sext(v24) dst_sel:DWORD dst_unused:UNUSED_PAD src0_sel:BYTE_1
	v_cvt_f32_i32_sdwa v51, sext(v25) dst_sel:DWORD dst_unused:UNUSED_PAD src0_sel:BYTE_1
	v_fmac_f32_e32 v59, v50, v4
	v_cvt_f32_i32_sdwa v50, sext(v26) dst_sel:DWORD dst_unused:UNUSED_PAD src0_sel:BYTE_1
	v_fmac_f32_e32 v59, v49, v1
	v_fmac_f32_e32 v59, v51, v9
	v_cvt_f32_i32_sdwa v49, sext(v27) dst_sel:DWORD dst_unused:UNUSED_PAD src0_sel:BYTE_1
	v_fmac_f32_e32 v59, v50, v13
	v_cvt_f32_i32_sdwa v50, sext(v24) dst_sel:DWORD dst_unused:UNUSED_PAD src0_sel:BYTE_2
	v_cvt_f32_i32_sdwa v51, sext(v25) dst_sel:DWORD dst_unused:UNUSED_PAD src0_sel:BYTE_2
	v_fmac_f32_e32 v59, v49, v5
	v_cvt_f32_i32_sdwa v49, sext(v26) dst_sel:DWORD dst_unused:UNUSED_PAD src0_sel:BYTE_2
	v_fmac_f32_e32 v59, v50, v2
	v_cvt_f32_i32_sdwa v50, sext(v27) dst_sel:DWORD dst_unused:UNUSED_PAD src0_sel:BYTE_2
	v_cvt_f32_i32_sdwa v24, sext(v24) dst_sel:DWORD dst_unused:UNUSED_PAD src0_sel:BYTE_3
	v_fmac_f32_e32 v59, v51, v10
	v_cvt_f32_i32_sdwa v25, sext(v25) dst_sel:DWORD dst_unused:UNUSED_PAD src0_sel:BYTE_3
	v_fmac_f32_e32 v59, v49, v14
	v_fmac_f32_e32 v59, v50, v6
	v_cvt_f32_i32_sdwa v61, sext(v27) dst_sel:DWORD dst_unused:UNUSED_PAD src0_sel:BYTE_3
	ds_bpermute_b32 v56, v44, v48 offset:224
	v_fmac_f32_e32 v59, v24, v3
	v_fmac_f32_e32 v59, v25, v11
	v_fmac_f32_e32 v59, v57, v15
	v_fmac_f32_e32 v59, v61, v7
	global_load_dwordx4 v[24:27], v[52:53], off
	global_load_dwordx4 v[48:51], v[54:55], off
	v_add_f32_dpp v53, v59, v59 quad_perm:[1,0,3,2] row_mask:0xf bank_mask:0xf bound_ctrl:1
	s_waitcnt lgkmcnt(0)
	v_ashrrev_i32_e32 v57, 31, v56
	v_lshlrev_b64 v[54:55], 7, v[56:57]
	v_add_f32_dpp v53, v53, v53 quad_perm:[2,3,0,1] row_mask:0xf bank_mask:0xf bound_ctrl:1
	ds_bpermute_b32 v52, v44, v47 offset:224
	v_add_u32_dpp v47, v60, v60 quad_perm:[1,0,3,2] row_mask:0xf bank_mask:0xf bound_ctrl:1
	v_add_f32_dpp v53, v53, v53 row_half_mirror row_mask:0xf bank_mask:0xf bound_ctrl:1
	s_waitcnt vmcnt(5)
	v_cvt_f32_i32_sdwa v56, sext(v16) dst_sel:DWORD dst_unused:UNUSED_PAD src0_sel:BYTE_0
	v_cndmask_b32_e64 v40, v40, v53, s[4:5]
	v_cvt_f32_i32_sdwa v53, sext(v17) dst_sel:DWORD dst_unused:UNUSED_PAD src0_sel:BYTE_0
	v_cvt_f32_i32_sdwa v57, sext(v18) dst_sel:DWORD dst_unused:UNUSED_PAD src0_sel:BYTE_0
	v_fma_f32 v56, v56, v0, 0
	v_add_u32_dpp v47, v47, v47 quad_perm:[2,3,0,1] row_mask:0xf bank_mask:0xf bound_ctrl:1
	v_fmac_f32_e32 v56, v53, v8
	v_cvt_f32_i32_sdwa v53, sext(v19) dst_sel:DWORD dst_unused:UNUSED_PAD src0_sel:BYTE_0
	v_add_u32_dpp v47, v47, v47 row_half_mirror row_mask:0xf bank_mask:0xf bound_ctrl:1
	v_fmac_f32_e32 v56, v57, v12
	v_cvt_f32_i32_sdwa v57, sext(v16) dst_sel:DWORD dst_unused:UNUSED_PAD src0_sel:BYTE_1
	v_cndmask_b32_e64 v47, v58, v47, s[4:5]
	v_cvt_f32_i32_sdwa v58, sext(v17) dst_sel:DWORD dst_unused:UNUSED_PAD src0_sel:BYTE_1
	v_fmac_f32_e32 v56, v53, v4
	v_fmac_f32_e32 v56, v57, v1
	v_cvt_f32_i32_sdwa v57, sext(v18) dst_sel:DWORD dst_unused:UNUSED_PAD src0_sel:BYTE_1
	v_fmac_f32_e32 v56, v58, v9
	v_cvt_f32_i32_sdwa v58, sext(v19) dst_sel:DWORD dst_unused:UNUSED_PAD src0_sel:BYTE_1
	s_waitcnt lgkmcnt(0)
	v_ashrrev_i32_e32 v53, 31, v52
	v_fmac_f32_e32 v56, v57, v13
	v_cvt_f32_i32_sdwa v57, sext(v16) dst_sel:DWORD dst_unused:UNUSED_PAD src0_sel:BYTE_2
	v_fmac_f32_e32 v56, v58, v5
	v_cvt_f32_i32_sdwa v58, sext(v17) dst_sel:DWORD dst_unused:UNUSED_PAD src0_sel:BYTE_2
	v_lshl_add_u64 v[54:55], v[42:43], 0, v[54:55]
	v_fmac_f32_e32 v56, v57, v2
	v_mov_b32_e32 v57, v41
	v_fmac_f32_e32 v56, v58, v10
	v_cvt_f32_i32_sdwa v58, sext(v18) dst_sel:DWORD dst_unused:UNUSED_PAD src0_sel:BYTE_2
	s_waitcnt vmcnt(4)
	v_dot4c_i32_i8_e32 v57, v16, v20
	v_dot4c_i32_i8_e32 v57, v17, v21
	v_lshlrev_b64 v[52:53], 7, v[52:53]
	v_dot4c_i32_i8_e32 v57, v18, v22
	v_lshl_add_u64 v[52:53], v[42:43], 0, v[52:53]
	v_fmac_f32_e32 v56, v58, v14
	v_cvt_f32_i32_sdwa v58, sext(v19) dst_sel:DWORD dst_unused:UNUSED_PAD src0_sel:BYTE_2
	v_dot4c_i32_i8_e32 v57, v19, v23
	v_cvt_f32_i32_sdwa v59, sext(v16) dst_sel:DWORD dst_unused:UNUSED_PAD src0_sel:BYTE_3
	v_cvt_f32_i32_sdwa v60, sext(v17) dst_sel:DWORD dst_unused:UNUSED_PAD src0_sel:BYTE_3
	v_cvt_f32_i32_sdwa v61, sext(v18) dst_sel:DWORD dst_unused:UNUSED_PAD src0_sel:BYTE_3
	v_cvt_f32_i32_sdwa v62, sext(v19) dst_sel:DWORD dst_unused:UNUSED_PAD src0_sel:BYTE_3
	global_load_dwordx4 v[16:19], v[54:55], off
	global_load_dwordx4 v[20:23], v[52:53], off
	v_fmac_f32_e32 v56, v58, v6
	v_fmac_f32_e32 v56, v59, v3
	v_add_u32_dpp v52, v57, v57 quad_perm:[1,0,3,2] row_mask:0xf bank_mask:0xf bound_ctrl:1
	v_fmac_f32_e32 v56, v60, v11
	v_fmac_f32_e32 v56, v61, v15
	v_add_u32_dpp v52, v52, v52 quad_perm:[2,3,0,1] row_mask:0xf bank_mask:0xf bound_ctrl:1
	v_fmac_f32_e32 v56, v62, v7
	s_waitcnt vmcnt(5)
	v_cvt_f32_i32_sdwa v54, sext(v35) dst_sel:DWORD dst_unused:UNUSED_PAD src0_sel:BYTE_1
	v_add_u32_dpp v52, v52, v52 row_half_mirror row_mask:0xf bank_mask:0xf bound_ctrl:1
	v_cndmask_b32_e64 v47, v47, v52, s[6:7]
	v_mov_b32_e32 v52, v41
	v_add_f32_dpp v53, v56, v56 quad_perm:[1,0,3,2] row_mask:0xf bank_mask:0xf bound_ctrl:1
	s_waitcnt vmcnt(4)
	v_dot4c_i32_i8_e32 v52, v32, v36
	v_cvt_f32_i32_sdwa v36, sext(v32) dst_sel:DWORD dst_unused:UNUSED_PAD src0_sel:BYTE_0
	v_add_f32_dpp v53, v53, v53 quad_perm:[2,3,0,1] row_mask:0xf bank_mask:0xf bound_ctrl:1
	v_dot4c_i32_i8_e32 v52, v33, v37
	v_cvt_f32_i32_sdwa v37, sext(v33) dst_sel:DWORD dst_unused:UNUSED_PAD src0_sel:BYTE_0
	v_add_f32_dpp v53, v53, v53 row_half_mirror row_mask:0xf bank_mask:0xf bound_ctrl:1
	v_dot4c_i32_i8_e32 v52, v34, v38
	v_cvt_f32_i32_sdwa v38, sext(v34) dst_sel:DWORD dst_unused:UNUSED_PAD src0_sel:BYTE_0
	v_cndmask_b32_e64 v40, v40, v53, s[6:7]
	v_cvt_f32_i32_sdwa v53, sext(v35) dst_sel:DWORD dst_unused:UNUSED_PAD src0_sel:BYTE_0
	v_fma_f32 v36, v36, v0, 0
	v_fmac_f32_e32 v36, v37, v8
	v_cvt_f32_i32_sdwa v37, sext(v32) dst_sel:DWORD dst_unused:UNUSED_PAD src0_sel:BYTE_1
	v_fmac_f32_e32 v36, v38, v12
	v_cvt_f32_i32_sdwa v38, sext(v33) dst_sel:DWORD dst_unused:UNUSED_PAD src0_sel:BYTE_1
	v_fmac_f32_e32 v36, v53, v4
	v_cvt_f32_i32_sdwa v53, sext(v34) dst_sel:DWORD dst_unused:UNUSED_PAD src0_sel:BYTE_1
	v_fmac_f32_e32 v36, v37, v1
	v_cvt_f32_i32_sdwa v37, sext(v32) dst_sel:DWORD dst_unused:UNUSED_PAD src0_sel:BYTE_2
	v_fmac_f32_e32 v36, v38, v9
	v_cvt_f32_i32_sdwa v38, sext(v33) dst_sel:DWORD dst_unused:UNUSED_PAD src0_sel:BYTE_2
	v_fmac_f32_e32 v36, v53, v13
	v_cvt_f32_i32_sdwa v53, sext(v34) dst_sel:DWORD dst_unused:UNUSED_PAD src0_sel:BYTE_2
	v_fmac_f32_e32 v36, v54, v5
	v_cvt_f32_i32_sdwa v54, sext(v35) dst_sel:DWORD dst_unused:UNUSED_PAD src0_sel:BYTE_2
	v_fmac_f32_e32 v36, v37, v2
	v_cvt_f32_i32_sdwa v32, sext(v32) dst_sel:DWORD dst_unused:UNUSED_PAD src0_sel:BYTE_3
	v_fmac_f32_e32 v36, v38, v10
	v_cvt_f32_i32_sdwa v33, sext(v33) dst_sel:DWORD dst_unused:UNUSED_PAD src0_sel:BYTE_3
	v_fmac_f32_e32 v36, v53, v14
	v_cvt_f32_i32_sdwa v34, sext(v34) dst_sel:DWORD dst_unused:UNUSED_PAD src0_sel:BYTE_3
	v_fmac_f32_e32 v36, v54, v6
	v_cvt_f32_i32_sdwa v37, sext(v35) dst_sel:DWORD dst_unused:UNUSED_PAD src0_sel:BYTE_3
	v_fmac_f32_e32 v36, v32, v3
	v_fmac_f32_e32 v36, v33, v11
	v_fmac_f32_e32 v36, v34, v15
	v_fmac_f32_e32 v36, v37, v7
	v_dot4c_i32_i8_e32 v52, v35, v39
	s_waitcnt vmcnt(3)
	v_cvt_f32_i32_sdwa v35, sext(v24) dst_sel:DWORD dst_unused:UNUSED_PAD src0_sel:BYTE_0
	v_add_f32_dpp v33, v36, v36 quad_perm:[1,0,3,2] row_mask:0xf bank_mask:0xf bound_ctrl:1
	v_cvt_f32_i32_sdwa v36, sext(v25) dst_sel:DWORD dst_unused:UNUSED_PAD src0_sel:BYTE_0
	v_cvt_f32_i32_sdwa v37, sext(v26) dst_sel:DWORD dst_unused:UNUSED_PAD src0_sel:BYTE_0
	v_cvt_f32_i32_sdwa v38, sext(v27) dst_sel:DWORD dst_unused:UNUSED_PAD src0_sel:BYTE_0
	v_fma_f32 v35, v35, v0, 0
	v_fmac_f32_e32 v35, v36, v8
	v_cvt_f32_i32_sdwa v36, sext(v24) dst_sel:DWORD dst_unused:UNUSED_PAD src0_sel:BYTE_1
	v_fmac_f32_e32 v35, v37, v12
	v_cvt_f32_i32_sdwa v37, sext(v25) dst_sel:DWORD dst_unused:UNUSED_PAD src0_sel:BYTE_1
	v_fmac_f32_e32 v35, v38, v4
	v_cvt_f32_i32_sdwa v38, sext(v26) dst_sel:DWORD dst_unused:UNUSED_PAD src0_sel:BYTE_1
	v_cvt_f32_i32_sdwa v39, sext(v27) dst_sel:DWORD dst_unused:UNUSED_PAD src0_sel:BYTE_1
	v_fmac_f32_e32 v35, v36, v1
	v_cvt_f32_i32_sdwa v36, sext(v24) dst_sel:DWORD dst_unused:UNUSED_PAD src0_sel:BYTE_2
	v_fmac_f32_e32 v35, v37, v9
	v_cvt_f32_i32_sdwa v37, sext(v25) dst_sel:DWORD dst_unused:UNUSED_PAD src0_sel:BYTE_2
	v_fmac_f32_e32 v35, v38, v13
	v_cvt_f32_i32_sdwa v38, sext(v26) dst_sel:DWORD dst_unused:UNUSED_PAD src0_sel:BYTE_2
	v_mov_b32_e32 v34, v41
	v_fmac_f32_e32 v35, v39, v5
	v_cvt_f32_i32_sdwa v39, sext(v27) dst_sel:DWORD dst_unused:UNUSED_PAD src0_sel:BYTE_2
	s_waitcnt vmcnt(2)
	v_dot4c_i32_i8_e32 v34, v24, v48
	v_fmac_f32_e32 v35, v36, v2
	v_cvt_f32_i32_sdwa v24, sext(v24) dst_sel:DWORD dst_unused:UNUSED_PAD src0_sel:BYTE_3
	v_dot4c_i32_i8_e32 v34, v25, v49
	v_fmac_f32_e32 v35, v37, v10
	v_cvt_f32_i32_sdwa v25, sext(v25) dst_sel:DWORD dst_unused:UNUSED_PAD src0_sel:BYTE_3
	v_dot4c_i32_i8_e32 v34, v26, v50
	v_fmac_f32_e32 v35, v38, v14
	v_cvt_f32_i32_sdwa v26, sext(v26) dst_sel:DWORD dst_unused:UNUSED_PAD src0_sel:BYTE_3
	v_fmac_f32_e32 v35, v39, v6
	v_fmac_f32_e32 v35, v24, v3
	v_fmac_f32_e32 v35, v25, v11
	v_fmac_f32_e32 v35, v26, v15
	v_mov_b32_e32 v26, v41
	s_waitcnt vmcnt(0)
	v_dot4c_i32_i8_e32 v26, v16, v20
	v_cvt_f32_i32_sdwa v20, sext(v16) dst_sel:DWORD dst_unused:UNUSED_PAD src0_sel:BYTE_0
	v_dot4c_i32_i8_e32 v26, v17, v21
	v_cvt_f32_i32_sdwa v21, sext(v17) dst_sel:DWORD dst_unused:UNUSED_PAD src0_sel:BYTE_0
	v_dot4c_i32_i8_e32 v26, v18, v22
	v_cvt_f32_i32_sdwa v22, sext(v18) dst_sel:DWORD dst_unused:UNUSED_PAD src0_sel:BYTE_0
	v_cvt_f32_i32_sdwa v36, sext(v27) dst_sel:DWORD dst_unused:UNUSED_PAD src0_sel:BYTE_3
	v_dot4c_i32_i8_e32 v34, v27, v51
	v_cvt_f32_i32_sdwa v27, sext(v19) dst_sel:DWORD dst_unused:UNUSED_PAD src0_sel:BYTE_0
	v_add_u32_dpp v32, v52, v52 quad_perm:[1,0,3,2] row_mask:0xf bank_mask:0xf bound_ctrl:1
	v_fma_f32 v20, v20, v0, 0
	v_add_u32_dpp v24, v34, v34 quad_perm:[1,0,3,2] row_mask:0xf bank_mask:0xf bound_ctrl:1
	v_add_u32_dpp v32, v32, v32 quad_perm:[2,3,0,1] row_mask:0xf bank_mask:0xf bound_ctrl:1
	v_fmac_f32_e32 v20, v21, v8
	v_cvt_f32_i32_sdwa v21, sext(v16) dst_sel:DWORD dst_unused:UNUSED_PAD src0_sel:BYTE_1
	v_add_u32_dpp v32, v32, v32 row_half_mirror row_mask:0xf bank_mask:0xf bound_ctrl:1
	v_add_u32_dpp v24, v24, v24 quad_perm:[2,3,0,1] row_mask:0xf bank_mask:0xf bound_ctrl:1
	v_fmac_f32_e32 v20, v22, v12
	v_cvt_f32_i32_sdwa v22, sext(v17) dst_sel:DWORD dst_unused:UNUSED_PAD src0_sel:BYTE_1
	v_cndmask_b32_e64 v32, v47, v32, s[8:9]
	v_add_u32_dpp v24, v24, v24 row_half_mirror row_mask:0xf bank_mask:0xf bound_ctrl:1
	v_fmac_f32_e32 v20, v27, v4
	v_cvt_f32_i32_sdwa v27, sext(v18) dst_sel:DWORD dst_unused:UNUSED_PAD src0_sel:BYTE_1
	v_cndmask_b32_e64 v24, v32, v24, s[10:11]
	v_cvt_f32_i32_sdwa v32, sext(v19) dst_sel:DWORD dst_unused:UNUSED_PAD src0_sel:BYTE_1
	v_fmac_f32_e32 v20, v21, v1
	v_cvt_f32_i32_sdwa v21, sext(v16) dst_sel:DWORD dst_unused:UNUSED_PAD src0_sel:BYTE_2
	v_fmac_f32_e32 v20, v22, v9
	v_cvt_f32_i32_sdwa v22, sext(v17) dst_sel:DWORD dst_unused:UNUSED_PAD src0_sel:BYTE_2
	v_fmac_f32_e32 v20, v27, v13
	v_cvt_f32_i32_sdwa v27, sext(v18) dst_sel:DWORD dst_unused:UNUSED_PAD src0_sel:BYTE_2
	v_fmac_f32_e32 v20, v32, v5
	v_cvt_f32_i32_sdwa v32, sext(v19) dst_sel:DWORD dst_unused:UNUSED_PAD src0_sel:BYTE_2
	v_fmac_f32_e32 v20, v21, v2
	v_cvt_f32_i32_sdwa v16, sext(v16) dst_sel:DWORD dst_unused:UNUSED_PAD src0_sel:BYTE_3
	v_fmac_f32_e32 v20, v22, v10
	v_cvt_f32_i32_sdwa v17, sext(v17) dst_sel:DWORD dst_unused:UNUSED_PAD src0_sel:BYTE_3
	v_fmac_f32_e32 v20, v27, v14
	v_cvt_f32_i32_sdwa v18, sext(v18) dst_sel:DWORD dst_unused:UNUSED_PAD src0_sel:BYTE_3
	v_fmac_f32_e32 v20, v32, v6
	v_cvt_f32_i32_sdwa v21, sext(v19) dst_sel:DWORD dst_unused:UNUSED_PAD src0_sel:BYTE_3
	v_dot4c_i32_i8_e32 v26, v19, v23
	v_fmac_f32_e32 v20, v16, v3
	v_fmac_f32_e32 v20, v17, v11
	v_fmac_f32_e32 v35, v36, v7
	v_add_u32_dpp v16, v26, v26 quad_perm:[1,0,3,2] row_mask:0xf bank_mask:0xf bound_ctrl:1
	v_fmac_f32_e32 v20, v18, v15
	v_add_f32_dpp v33, v33, v33 quad_perm:[2,3,0,1] row_mask:0xf bank_mask:0xf bound_ctrl:1
	v_add_u32_dpp v16, v16, v16 quad_perm:[2,3,0,1] row_mask:0xf bank_mask:0xf bound_ctrl:1
	v_add_f32_dpp v25, v35, v35 quad_perm:[1,0,3,2] row_mask:0xf bank_mask:0xf bound_ctrl:1
	v_fmac_f32_e32 v20, v21, v7
	v_add_u32_dpp v18, v16, v16 row_half_mirror row_mask:0xf bank_mask:0xf bound_ctrl:1
	ds_bpermute_b32 v16, v44, v45
	v_cndmask_b32_e64 v18, v24, v18, s[12:13]
	v_add_f32_dpp v33, v33, v33 row_half_mirror row_mask:0xf bank_mask:0xf bound_ctrl:1
	v_add_f32_dpp v25, v25, v25 quad_perm:[2,3,0,1] row_mask:0xf bank_mask:0xf bound_ctrl:1
	v_add_f32_dpp v17, v20, v20 quad_perm:[1,0,3,2] row_mask:0xf bank_mask:0xf bound_ctrl:1
	global_store_dword v[28:29], v18, off offset:512
	ds_bpermute_b32 v18, v44, v46
	v_cndmask_b32_e64 v33, v40, v33, s[8:9]
	v_add_f32_dpp v25, v25, v25 row_half_mirror row_mask:0xf bank_mask:0xf bound_ctrl:1
	v_add_f32_dpp v17, v17, v17 quad_perm:[2,3,0,1] row_mask:0xf bank_mask:0xf bound_ctrl:1
	v_cndmask_b32_e64 v25, v33, v25, s[10:11]
	s_waitcnt lgkmcnt(0)
	v_ashrrev_i32_e32 v19, 31, v18
	v_add_f32_dpp v17, v17, v17 row_half_mirror row_mask:0xf bank_mask:0xf bound_ctrl:1
	v_cndmask_b32_e64 v17, v25, v17, s[12:13]
	global_store_dword v[30:31], v17, off offset:512
	v_ashrrev_i32_e32 v17, 31, v16
	v_lshlrev_b64 v[16:17], 7, v[16:17]
	v_lshl_add_u64 v[16:17], v[42:43], 0, v[16:17]
	v_lshlrev_b64 v[18:19], 7, v[18:19]
	v_lshl_add_u64 v[18:19], v[42:43], 0, v[18:19]
	global_load_dwordx4 v[32:35], v[16:17], off
	global_load_dwordx4 v[36:39], v[18:19], off
	ds_bpermute_b32 v16, v44, v45 offset:32
	ds_bpermute_b32 v18, v44, v46 offset:32
	v_mov_b32_e32 v66, v41
	v_mov_b32_e32 v40, v41
	s_waitcnt lgkmcnt(1)
	v_ashrrev_i32_e32 v17, 31, v16
	v_lshlrev_b64 v[16:17], 7, v[16:17]
	s_waitcnt lgkmcnt(0)
	v_ashrrev_i32_e32 v19, 31, v18
	v_lshl_add_u64 v[16:17], v[42:43], 0, v[16:17]
	v_lshlrev_b64 v[18:19], 7, v[18:19]
	v_lshl_add_u64 v[18:19], v[42:43], 0, v[18:19]
	global_load_dwordx4 v[20:23], v[16:17], off
	global_load_dwordx4 v[48:51], v[18:19], off
	ds_bpermute_b32 v16, v44, v45 offset:64
	ds_bpermute_b32 v18, v44, v46 offset:64
	s_waitcnt lgkmcnt(1)
	v_ashrrev_i32_e32 v17, 31, v16
	v_lshlrev_b64 v[16:17], 7, v[16:17]
	s_waitcnt lgkmcnt(0)
	v_ashrrev_i32_e32 v19, 31, v18
	v_lshl_add_u64 v[52:53], v[42:43], 0, v[16:17]
	v_lshlrev_b64 v[16:17], 7, v[18:19]
	v_lshl_add_u64 v[54:55], v[42:43], 0, v[16:17]
	global_load_dwordx4 v[16:19], v[52:53], off
	global_load_dwordx4 v[24:27], v[54:55], off
	s_waitcnt vmcnt(5)
	v_cvt_f32_i32_sdwa v47, sext(v33) dst_sel:DWORD dst_unused:UNUSED_PAD src0_sel:BYTE_0
	s_waitcnt vmcnt(4)
	v_dot4c_i32_i8_e32 v40, v32, v36
	v_dot4c_i32_i8_e32 v40, v33, v37
	v_dot4c_i32_i8_e32 v40, v34, v38
	v_cvt_f32_i32_sdwa v38, sext(v32) dst_sel:DWORD dst_unused:UNUSED_PAD src0_sel:BYTE_0
	v_cvt_f32_i32_sdwa v60, sext(v32) dst_sel:DWORD dst_unused:UNUSED_PAD src0_sel:BYTE_1
	v_cvt_f32_i32_sdwa v61, sext(v33) dst_sel:DWORD dst_unused:UNUSED_PAD src0_sel:BYTE_1
	v_dot4c_i32_i8_e32 v40, v35, v39
	v_cvt_f32_i32_sdwa v39, sext(v32) dst_sel:DWORD dst_unused:UNUSED_PAD src0_sel:BYTE_2
	v_cvt_f32_i32_sdwa v64, sext(v33) dst_sel:DWORD dst_unused:UNUSED_PAD src0_sel:BYTE_2
	v_cvt_f32_i32_sdwa v67, sext(v33) dst_sel:DWORD dst_unused:UNUSED_PAD src0_sel:BYTE_3
	v_cvt_f32_i32_sdwa v58, sext(v34) dst_sel:DWORD dst_unused:UNUSED_PAD src0_sel:BYTE_0
	s_waitcnt vmcnt(3)
	v_cvt_f32_i32_sdwa v68, sext(v20) dst_sel:DWORD dst_unused:UNUSED_PAD src0_sel:BYTE_0
	s_waitcnt vmcnt(2)
	v_dot4c_i32_i8_e32 v66, v20, v48
	v_dot4c_i32_i8_e32 v66, v21, v49
	v_cvt_f32_i32_sdwa v69, sext(v21) dst_sel:DWORD dst_unused:UNUSED_PAD src0_sel:BYTE_0
	v_cvt_f32_i32_sdwa v73, sext(v20) dst_sel:DWORD dst_unused:UNUSED_PAD src0_sel:BYTE_1
	v_cvt_f32_i32_sdwa v74, sext(v21) dst_sel:DWORD dst_unused:UNUSED_PAD src0_sel:BYTE_1
	v_cvt_f32_i32_sdwa v77, sext(v20) dst_sel:DWORD dst_unused:UNUSED_PAD src0_sel:BYTE_2
	v_cvt_f32_i32_sdwa v78, sext(v21) dst_sel:DWORD dst_unused:UNUSED_PAD src0_sel:BYTE_2
	v_cvt_f32_i32_sdwa v81, sext(v20) dst_sel:DWORD dst_unused:UNUSED_PAD src0_sel:BYTE_3
	v_cvt_f32_i32_sdwa v82, sext(v21) dst_sel:DWORD dst_unused:UNUSED_PAD src0_sel:BYTE_3
	v_cvt_f32_i32_sdwa v49, sext(v32) dst_sel:DWORD dst_unused:UNUSED_PAD src0_sel:BYTE_3
	v_dot4c_i32_i8_e32 v66, v22, v50
	s_waitcnt vmcnt(1)
	v_cvt_f32_i32_sdwa v85, sext(v16) dst_sel:DWORD dst_unused:UNUSED_PAD src0_sel:BYTE_0
	s_waitcnt vmcnt(0)
	v_dot4c_i32_i8_e32 v70, v16, v24
	v_dot4c_i32_i8_e32 v70, v17, v25
	v_cvt_f32_i32_sdwa v89, sext(v16) dst_sel:DWORD dst_unused:UNUSED_PAD src0_sel:BYTE_1
	v_cvt_f32_i32_sdwa v93, sext(v16) dst_sel:DWORD dst_unused:UNUSED_PAD src0_sel:BYTE_2
	v_cvt_f32_i32_sdwa v97, sext(v16) dst_sel:DWORD dst_unused:UNUSED_PAD src0_sel:BYTE_3
	ds_bpermute_b32 v16, v44, v45 offset:96
	v_dot4c_i32_i8_e32 v70, v18, v26
	v_cvt_f32_i32_sdwa v87, sext(v18) dst_sel:DWORD dst_unused:UNUSED_PAD src0_sel:BYTE_0
	v_cvt_f32_i32_sdwa v91, sext(v18) dst_sel:DWORD dst_unused:UNUSED_PAD src0_sel:BYTE_1
	v_cvt_f32_i32_sdwa v95, sext(v18) dst_sel:DWORD dst_unused:UNUSED_PAD src0_sel:BYTE_2
	v_cvt_f32_i32_sdwa v99, sext(v18) dst_sel:DWORD dst_unused:UNUSED_PAD src0_sel:BYTE_3
	ds_bpermute_b32 v18, v44, v46 offset:96
	v_cvt_f32_i32_sdwa v86, sext(v17) dst_sel:DWORD dst_unused:UNUSED_PAD src0_sel:BYTE_0
	v_cvt_f32_i32_sdwa v90, sext(v17) dst_sel:DWORD dst_unused:UNUSED_PAD src0_sel:BYTE_1
	v_cvt_f32_i32_sdwa v94, sext(v17) dst_sel:DWORD dst_unused:UNUSED_PAD src0_sel:BYTE_2
	v_cvt_f32_i32_sdwa v98, sext(v17) dst_sel:DWORD dst_unused:UNUSED_PAD src0_sel:BYTE_3
	s_waitcnt lgkmcnt(1)
	v_ashrrev_i32_e32 v17, 31, v16
	v_dot4c_i32_i8_e32 v70, v19, v27
	v_cvt_f32_i32_sdwa v88, sext(v19) dst_sel:DWORD dst_unused:UNUSED_PAD src0_sel:BYTE_0
	v_cvt_f32_i32_sdwa v92, sext(v19) dst_sel:DWORD dst_unused:UNUSED_PAD src0_sel:BYTE_1
	v_cvt_f32_i32_sdwa v96, sext(v19) dst_sel:DWORD dst_unused:UNUSED_PAD src0_sel:BYTE_2
	v_cvt_f32_i32_sdwa v100, sext(v19) dst_sel:DWORD dst_unused:UNUSED_PAD src0_sel:BYTE_3
	v_lshlrev_b64 v[16:17], 7, v[16:17]
	s_waitcnt lgkmcnt(0)
	v_ashrrev_i32_e32 v19, 31, v18
	v_lshl_add_u64 v[20:21], v[42:43], 0, v[16:17]
	ds_bpermute_b32 v16, v44, v45 offset:128
	v_lshlrev_b64 v[18:19], 7, v[18:19]
	v_lshl_add_u64 v[24:25], v[42:43], 0, v[18:19]
	ds_bpermute_b32 v18, v44, v46 offset:128
	v_cvt_f32_i32_sdwa v71, sext(v22) dst_sel:DWORD dst_unused:UNUSED_PAD src0_sel:BYTE_0
	s_waitcnt lgkmcnt(1)
	v_ashrrev_i32_e32 v17, 31, v16
	v_lshlrev_b64 v[16:17], 7, v[16:17]
	v_lshl_add_u64 v[32:33], v[42:43], 0, v[16:17]
	s_waitcnt lgkmcnt(0)
	v_ashrrev_i32_e32 v19, 31, v18
	ds_bpermute_b32 v16, v44, v45 offset:160
	v_lshlrev_b64 v[18:19], 7, v[18:19]
	v_lshl_add_u64 v[36:37], v[42:43], 0, v[18:19]
	ds_bpermute_b32 v18, v44, v46 offset:160
	v_cvt_f32_i32_sdwa v75, sext(v22) dst_sel:DWORD dst_unused:UNUSED_PAD src0_sel:BYTE_1
	v_cvt_f32_i32_sdwa v79, sext(v22) dst_sel:DWORD dst_unused:UNUSED_PAD src0_sel:BYTE_2
	v_cvt_f32_i32_sdwa v83, sext(v22) dst_sel:DWORD dst_unused:UNUSED_PAD src0_sel:BYTE_3
	ds_bpermute_b32 v22, v44, v45 offset:192
	s_waitcnt lgkmcnt(2)
	v_ashrrev_i32_e32 v17, 31, v16
	v_lshlrev_b64 v[16:17], 7, v[16:17]
	s_waitcnt lgkmcnt(1)
	v_ashrrev_i32_e32 v19, 31, v18
	v_dot4c_i32_i8_e32 v66, v23, v51
	v_cvt_f32_i32_sdwa v72, sext(v23) dst_sel:DWORD dst_unused:UNUSED_PAD src0_sel:BYTE_0
	v_cvt_f32_i32_sdwa v76, sext(v23) dst_sel:DWORD dst_unused:UNUSED_PAD src0_sel:BYTE_1
	v_cvt_f32_i32_sdwa v80, sext(v23) dst_sel:DWORD dst_unused:UNUSED_PAD src0_sel:BYTE_2
	v_cvt_f32_i32_sdwa v84, sext(v23) dst_sel:DWORD dst_unused:UNUSED_PAD src0_sel:BYTE_3
	v_lshl_add_u64 v[50:51], v[42:43], 0, v[16:17]
	v_lshlrev_b64 v[16:17], 7, v[18:19]
	s_waitcnt lgkmcnt(0)
	v_ashrrev_i32_e32 v23, 31, v22
	v_lshl_add_u64 v[52:53], v[42:43], 0, v[16:17]
	v_lshlrev_b64 v[16:17], 7, v[22:23]
	v_lshl_add_u64 v[54:55], v[42:43], 0, v[16:17]
	ds_bpermute_b32 v16, v44, v46 offset:192
	ds_bpermute_b32 v18, v44, v45 offset:224
	ds_bpermute_b32 v22, v44, v46 offset:224
	v_cvt_f32_i32_sdwa v59, sext(v35) dst_sel:DWORD dst_unused:UNUSED_PAD src0_sel:BYTE_0
	v_fma_f32 v38, v38, v0, 0
	s_waitcnt lgkmcnt(2)
	v_ashrrev_i32_e32 v17, 31, v16
	v_lshlrev_b64 v[16:17], 7, v[16:17]
	s_waitcnt lgkmcnt(1)
	v_ashrrev_i32_e32 v19, 31, v18
	s_waitcnt lgkmcnt(0)
	v_ashrrev_i32_e32 v23, 31, v22
	v_lshl_add_u64 v[56:57], v[42:43], 0, v[16:17]
	v_lshlrev_b64 v[16:17], 7, v[18:19]
	v_lshlrev_b64 v[18:19], 7, v[22:23]
	global_load_dwordx4 v[20:23], v[20:21], off
	v_fmac_f32_e32 v38, v47, v8
	v_cvt_f32_i32_sdwa v62, sext(v34) dst_sel:DWORD dst_unused:UNUSED_PAD src0_sel:BYTE_1
	v_fmac_f32_e32 v38, v58, v12
	v_cvt_f32_i32_sdwa v63, sext(v35) dst_sel:DWORD dst_unused:UNUSED_PAD src0_sel:BYTE_1
	v_fmac_f32_e32 v38, v59, v4
	v_fmac_f32_e32 v38, v60, v1
	v_fmac_f32_e32 v38, v61, v9
	v_cvt_f32_i32_sdwa v65, sext(v34) dst_sel:DWORD dst_unused:UNUSED_PAD src0_sel:BYTE_2
	v_fmac_f32_e32 v38, v62, v13
	v_cvt_f32_i32_sdwa v48, sext(v35) dst_sel:DWORD dst_unused:UNUSED_PAD src0_sel:BYTE_2
	v_fmac_f32_e32 v38, v63, v5
	v_fmac_f32_e32 v38, v39, v2
	v_fmac_f32_e32 v38, v64, v10
	v_cvt_f32_i32_sdwa v34, sext(v34) dst_sel:DWORD dst_unused:UNUSED_PAD src0_sel:BYTE_3
	v_fmac_f32_e32 v38, v65, v14
	v_fmac_f32_e32 v38, v48, v6
	v_fmac_f32_e32 v38, v49, v3
	v_fmac_f32_e32 v38, v67, v11
	v_fmac_f32_e32 v38, v34, v15
	v_fma_f32 v34, v68, v0, 0
	v_fmac_f32_e32 v34, v69, v8
	v_fmac_f32_e32 v34, v71, v12
	v_fmac_f32_e32 v34, v72, v4
	global_load_dwordx4 v[24:27], v[24:25], off
	v_fmac_f32_e32 v34, v73, v1
	v_fmac_f32_e32 v34, v74, v9
	v_fmac_f32_e32 v34, v75, v13
	v_fmac_f32_e32 v34, v76, v5
	v_fmac_f32_e32 v34, v77, v2
	v_fmac_f32_e32 v34, v78, v10
	v_cvt_f32_i32_sdwa v35, sext(v35) dst_sel:DWORD dst_unused:UNUSED_PAD src0_sel:BYTE_3
	v_fmac_f32_e32 v34, v79, v14
	v_fmac_f32_e32 v34, v80, v6
	v_fmac_f32_e32 v34, v81, v3
	v_fmac_f32_e32 v34, v82, v11
	v_fmac_f32_e32 v38, v35, v7
	v_fmac_f32_e32 v34, v83, v15
	v_fmac_f32_e32 v34, v84, v7
	v_add_f32_dpp v35, v38, v38 quad_perm:[1,0,3,2] row_mask:0xf bank_mask:0xf bound_ctrl:1
	v_lshl_add_u64 v[16:17], v[42:43], 0, v[16:17]
	v_add_f32_dpp v34, v34, v34 quad_perm:[1,0,3,2] row_mask:0xf bank_mask:0xf bound_ctrl:1
	v_add_f32_dpp v35, v35, v35 quad_perm:[2,3,0,1] row_mask:0xf bank_mask:0xf bound_ctrl:1
	v_lshl_add_u64 v[18:19], v[42:43], 0, v[18:19]
	v_add_f32_dpp v34, v34, v34 quad_perm:[2,3,0,1] row_mask:0xf bank_mask:0xf bound_ctrl:1
	v_add_f32_dpp v35, v35, v35 row_half_mirror row_mask:0xf bank_mask:0xf bound_ctrl:1
	v_cndmask_b32_e32 v35, 0, v35, vcc
	v_add_f32_dpp v34, v34, v34 row_half_mirror row_mask:0xf bank_mask:0xf bound_ctrl:1
	v_cndmask_b32_e64 v42, v35, v34, s[0:1]
	global_load_dwordx4 v[32:35], v[32:33], off
	v_fma_f32 v43, v85, v0, 0
	v_fmac_f32_e32 v43, v86, v8
	v_fmac_f32_e32 v43, v87, v12
	v_fmac_f32_e32 v43, v88, v4
	v_fmac_f32_e32 v43, v89, v1
	v_fmac_f32_e32 v43, v90, v9
	v_fmac_f32_e32 v43, v91, v13
	v_fmac_f32_e32 v43, v92, v5
	v_fmac_f32_e32 v43, v93, v2
	v_fmac_f32_e32 v43, v94, v10
	v_fmac_f32_e32 v43, v95, v14
	v_fmac_f32_e32 v43, v96, v6
	v_fmac_f32_e32 v43, v97, v3
	v_fmac_f32_e32 v43, v98, v11
	v_fmac_f32_e32 v43, v99, v15
	v_fmac_f32_e32 v43, v100, v7
	v_add_u32_dpp v38, v40, v40 quad_perm:[1,0,3,2] row_mask:0xf bank_mask:0xf bound_ctrl:1
	v_add_u32_dpp v39, v66, v66 quad_perm:[1,0,3,2] row_mask:0xf bank_mask:0xf bound_ctrl:1
	v_add_f32_dpp v43, v43, v43 quad_perm:[1,0,3,2] row_mask:0xf bank_mask:0xf bound_ctrl:1
	v_add_u32_dpp v38, v38, v38 quad_perm:[2,3,0,1] row_mask:0xf bank_mask:0xf bound_ctrl:1
	v_add_u32_dpp v39, v39, v39 quad_perm:[2,3,0,1] row_mask:0xf bank_mask:0xf bound_ctrl:1
	v_add_f32_dpp v43, v43, v43 quad_perm:[2,3,0,1] row_mask:0xf bank_mask:0xf bound_ctrl:1
	v_add_u32_dpp v38, v38, v38 row_half_mirror row_mask:0xf bank_mask:0xf bound_ctrl:1
	v_add_u32_dpp v44, v70, v70 quad_perm:[1,0,3,2] row_mask:0xf bank_mask:0xf bound_ctrl:1
	v_add_f32_dpp v43, v43, v43 row_half_mirror row_mask:0xf bank_mask:0xf bound_ctrl:1
	v_cndmask_b32_e64 v58, v42, v43, s[2:3]
	v_cndmask_b32_e32 v38, 0, v38, vcc
	v_add_u32_dpp v39, v39, v39 row_half_mirror row_mask:0xf bank_mask:0xf bound_ctrl:1
	v_add_u32_dpp v44, v44, v44 quad_perm:[2,3,0,1] row_mask:0xf bank_mask:0xf bound_ctrl:1
	v_cndmask_b32_e64 v40, v38, v39, s[0:1]
	s_waitcnt vmcnt(2)
	v_cvt_f32_i32_sdwa v42, sext(v20) dst_sel:DWORD dst_unused:UNUSED_PAD src0_sel:BYTE_0
	v_cvt_f32_i32_sdwa v43, sext(v21) dst_sel:DWORD dst_unused:UNUSED_PAD src0_sel:BYTE_0
	v_cvt_f32_i32_sdwa v45, sext(v22) dst_sel:DWORD dst_unused:UNUSED_PAD src0_sel:BYTE_0
	v_add_u32_dpp v44, v44, v44 row_half_mirror row_mask:0xf bank_mask:0xf bound_ctrl:1
	v_fma_f32 v59, v42, v0, 0
	v_fmac_f32_e32 v59, v43, v8
	global_load_dwordx4 v[36:39], v[36:37], off
	v_cndmask_b32_e64 v40, v40, v44, s[2:3]
	v_fmac_f32_e32 v59, v45, v12
	global_load_dwordx4 v[42:45], v[50:51], off
	global_load_dwordx4 v[46:49], v[52:53], off
	v_cvt_f32_i32_sdwa v60, sext(v23) dst_sel:DWORD dst_unused:UNUSED_PAD src0_sel:BYTE_0
	v_cvt_f32_i32_sdwa v61, sext(v20) dst_sel:DWORD dst_unused:UNUSED_PAD src0_sel:BYTE_1
	v_cvt_f32_i32_sdwa v62, sext(v21) dst_sel:DWORD dst_unused:UNUSED_PAD src0_sel:BYTE_1
	v_cvt_f32_i32_sdwa v50, sext(v22) dst_sel:DWORD dst_unused:UNUSED_PAD src0_sel:BYTE_1
	v_fmac_f32_e32 v59, v60, v4
	v_fmac_f32_e32 v59, v61, v1
	v_cvt_f32_i32_sdwa v51, sext(v23) dst_sel:DWORD dst_unused:UNUSED_PAD src0_sel:BYTE_1
	v_mov_b32_e32 v52, v41
	v_fmac_f32_e32 v59, v62, v9
	v_fmac_f32_e32 v59, v50, v13
	v_cvt_f32_i32_sdwa v50, sext(v21) dst_sel:DWORD dst_unused:UNUSED_PAD src0_sel:BYTE_2
	v_fmac_f32_e32 v59, v51, v5
	v_cvt_f32_i32_sdwa v51, sext(v23) dst_sel:DWORD dst_unused:UNUSED_PAD src0_sel:BYTE_2
	v_cvt_f32_i32_sdwa v53, sext(v20) dst_sel:DWORD dst_unused:UNUSED_PAD src0_sel:BYTE_3
	s_waitcnt vmcnt(4)
	v_dot4c_i32_i8_e32 v52, v20, v24
	v_cvt_f32_i32_sdwa v24, sext(v20) dst_sel:DWORD dst_unused:UNUSED_PAD src0_sel:BYTE_2
	v_dot4c_i32_i8_e32 v52, v21, v25
	v_dot4c_i32_i8_e32 v52, v22, v26
	v_dot4c_i32_i8_e32 v52, v23, v27
	v_fmac_f32_e32 v59, v24, v2
	v_fmac_f32_e32 v59, v50, v10
	v_cvt_f32_i32_sdwa v50, sext(v22) dst_sel:DWORD dst_unused:UNUSED_PAD src0_sel:BYTE_2
	v_cvt_f32_i32_sdwa v60, sext(v21) dst_sel:DWORD dst_unused:UNUSED_PAD src0_sel:BYTE_3
	v_cvt_f32_i32_sdwa v61, sext(v22) dst_sel:DWORD dst_unused:UNUSED_PAD src0_sel:BYTE_3
	v_cvt_f32_i32_sdwa v62, sext(v23) dst_sel:DWORD dst_unused:UNUSED_PAD src0_sel:BYTE_3
	global_load_dwordx4 v[20:23], v[54:55], off
	global_load_dwordx4 v[24:27], v[56:57], off
	v_fmac_f32_e32 v59, v50, v14
	v_fmac_f32_e32 v59, v51, v6
	v_fmac_f32_e32 v59, v53, v3
	v_fmac_f32_e32 v59, v60, v11
	v_fmac_f32_e32 v59, v61, v15
	v_fmac_f32_e32 v59, v62, v7
	v_add_u32_dpp v50, v52, v52 quad_perm:[1,0,3,2] row_mask:0xf bank_mask:0xf bound_ctrl:1
	s_waitcnt vmcnt(5)
	v_cvt_f32_i32_sdwa v52, sext(v32) dst_sel:DWORD dst_unused:UNUSED_PAD src0_sel:BYTE_0
	v_add_u32_dpp v50, v50, v50 quad_perm:[2,3,0,1] row_mask:0xf bank_mask:0xf bound_ctrl:1
	v_add_f32_dpp v51, v59, v59 quad_perm:[1,0,3,2] row_mask:0xf bank_mask:0xf bound_ctrl:1
	v_cvt_f32_i32_sdwa v53, sext(v32) dst_sel:DWORD dst_unused:UNUSED_PAD src0_sel:BYTE_1
	v_add_u32_dpp v50, v50, v50 row_half_mirror row_mask:0xf bank_mask:0xf bound_ctrl:1
	v_add_f32_dpp v51, v51, v51 quad_perm:[2,3,0,1] row_mask:0xf bank_mask:0xf bound_ctrl:1
	v_cndmask_b32_e64 v40, v40, v50, s[4:5]
	v_cvt_f32_i32_sdwa v50, sext(v33) dst_sel:DWORD dst_unused:UNUSED_PAD src0_sel:BYTE_0
	v_add_f32_dpp v51, v51, v51 row_half_mirror row_mask:0xf bank_mask:0xf bound_ctrl:1
	v_cndmask_b32_e64 v58, v58, v51, s[4:5]
	v_cvt_f32_i32_sdwa v51, sext(v34) dst_sel:DWORD dst_unused:UNUSED_PAD src0_sel:BYTE_0
	v_fma_f32 v59, v52, v0, 0
	v_cvt_f32_i32_sdwa v52, sext(v35) dst_sel:DWORD dst_unused:UNUSED_PAD src0_sel:BYTE_0
	v_fmac_f32_e32 v59, v50, v8
	v_cvt_f32_i32_sdwa v50, sext(v33) dst_sel:DWORD dst_unused:UNUSED_PAD src0_sel:BYTE_1
	v_fmac_f32_e32 v59, v51, v12
	v_cvt_f32_i32_sdwa v51, sext(v34) dst_sel:DWORD dst_unused:UNUSED_PAD src0_sel:BYTE_1
	v_fmac_f32_e32 v59, v52, v4
	v_cvt_f32_i32_sdwa v52, sext(v35) dst_sel:DWORD dst_unused:UNUSED_PAD src0_sel:BYTE_1
	v_fmac_f32_e32 v59, v53, v1
	v_cvt_f32_i32_sdwa v53, sext(v32) dst_sel:DWORD dst_unused:UNUSED_PAD src0_sel:BYTE_2
	v_fmac_f32_e32 v59, v50, v9
	v_fmac_f32_e32 v59, v51, v13
	v_fmac_f32_e32 v59, v52, v5
	v_fmac_f32_e32 v59, v53, v2
	global_load_dwordx4 v[50:53], v[16:17], off
	global_load_dwordx4 v[54:57], v[18:19], off
	v_cvt_f32_i32_sdwa v60, sext(v33) dst_sel:DWORD dst_unused:UNUSED_PAD src0_sel:BYTE_2
	v_cvt_f32_i32_sdwa v61, sext(v34) dst_sel:DWORD dst_unused:UNUSED_PAD src0_sel:BYTE_2
	v_cvt_f32_i32_sdwa v62, sext(v35) dst_sel:DWORD dst_unused:UNUSED_PAD src0_sel:BYTE_2
	v_cvt_f32_i32_sdwa v16, sext(v32) dst_sel:DWORD dst_unused:UNUSED_PAD src0_sel:BYTE_3
	v_fmac_f32_e32 v59, v60, v10
	v_mov_b32_e32 v18, v41
	v_fmac_f32_e32 v59, v61, v14
	v_fmac_f32_e32 v59, v62, v6
	v_cvt_f32_i32_sdwa v17, sext(v33) dst_sel:DWORD dst_unused:UNUSED_PAD src0_sel:BYTE_3
	v_fmac_f32_e32 v59, v16, v3
	v_cvt_f32_i32_sdwa v16, sext(v34) dst_sel:DWORD dst_unused:UNUSED_PAD src0_sel:BYTE_3
	s_waitcnt vmcnt(6)
	v_dot4c_i32_i8_e32 v18, v32, v36
	v_dot4c_i32_i8_e32 v18, v33, v37
	s_waitcnt vmcnt(5)
	v_cvt_f32_i32_sdwa v19, sext(v42) dst_sel:DWORD dst_unused:UNUSED_PAD src0_sel:BYTE_0
	v_cvt_f32_i32_sdwa v32, sext(v43) dst_sel:DWORD dst_unused:UNUSED_PAD src0_sel:BYTE_0
	v_cvt_f32_i32_sdwa v33, sext(v44) dst_sel:DWORD dst_unused:UNUSED_PAD src0_sel:BYTE_0
	v_dot4c_i32_i8_e32 v18, v34, v38
	v_cvt_f32_i32_sdwa v34, sext(v45) dst_sel:DWORD dst_unused:UNUSED_PAD src0_sel:BYTE_0
	v_fma_f32 v19, v19, v0, 0
	v_fmac_f32_e32 v19, v32, v8
	v_cvt_f32_i32_sdwa v32, sext(v42) dst_sel:DWORD dst_unused:UNUSED_PAD src0_sel:BYTE_1
	v_fmac_f32_e32 v19, v33, v12
	v_cvt_f32_i32_sdwa v33, sext(v43) dst_sel:DWORD dst_unused:UNUSED_PAD src0_sel:BYTE_1
	v_fmac_f32_e32 v19, v34, v4
	v_cvt_f32_i32_sdwa v34, sext(v44) dst_sel:DWORD dst_unused:UNUSED_PAD src0_sel:BYTE_1
	v_fmac_f32_e32 v59, v17, v11
	v_cvt_f32_i32_sdwa v17, sext(v35) dst_sel:DWORD dst_unused:UNUSED_PAD src0_sel:BYTE_3
	v_dot4c_i32_i8_e32 v18, v35, v39
	v_cvt_f32_i32_sdwa v35, sext(v45) dst_sel:DWORD dst_unused:UNUSED_PAD src0_sel:BYTE_1
	v_fmac_f32_e32 v19, v32, v1
	v_cvt_f32_i32_sdwa v32, sext(v42) dst_sel:DWORD dst_unused:UNUSED_PAD src0_sel:BYTE_2
	v_fmac_f32_e32 v19, v33, v9
	v_cvt_f32_i32_sdwa v33, sext(v43) dst_sel:DWORD dst_unused:UNUSED_PAD src0_sel:BYTE_2
	v_fmac_f32_e32 v19, v34, v13
	v_cvt_f32_i32_sdwa v34, sext(v44) dst_sel:DWORD dst_unused:UNUSED_PAD src0_sel:BYTE_2
	v_fmac_f32_e32 v19, v35, v5
	v_cvt_f32_i32_sdwa v35, sext(v45) dst_sel:DWORD dst_unused:UNUSED_PAD src0_sel:BYTE_2
	v_fmac_f32_e32 v19, v32, v2
	v_cvt_f32_i32_sdwa v32, sext(v42) dst_sel:DWORD dst_unused:UNUSED_PAD src0_sel:BYTE_3
	v_fmac_f32_e32 v19, v33, v10
	v_cvt_f32_i32_sdwa v33, sext(v43) dst_sel:DWORD dst_unused:UNUSED_PAD src0_sel:BYTE_3
	v_fmac_f32_e32 v19, v34, v14
	v_cvt_f32_i32_sdwa v34, sext(v44) dst_sel:DWORD dst_unused:UNUSED_PAD src0_sel:BYTE_3
	v_fmac_f32_e32 v59, v16, v15
	v_add_u32_dpp v16, v18, v18 quad_perm:[1,0,3,2] row_mask:0xf bank_mask:0xf bound_ctrl:1
	v_mov_b32_e32 v18, v41
	v_fmac_f32_e32 v19, v35, v6
	v_cvt_f32_i32_sdwa v35, sext(v45) dst_sel:DWORD dst_unused:UNUSED_PAD src0_sel:BYTE_3
	s_waitcnt vmcnt(4)
	v_dot4c_i32_i8_e32 v18, v42, v46
	v_fmac_f32_e32 v19, v32, v3
	v_dot4c_i32_i8_e32 v18, v43, v47
	v_fmac_f32_e32 v19, v33, v11
	v_fmac_f32_e32 v59, v17, v7
	v_dot4c_i32_i8_e32 v18, v44, v48
	v_fmac_f32_e32 v19, v34, v15
	v_add_f32_dpp v17, v59, v59 quad_perm:[1,0,3,2] row_mask:0xf bank_mask:0xf bound_ctrl:1
	v_fmac_f32_e32 v19, v35, v7
	v_dot4c_i32_i8_e32 v18, v45, v49
	v_add_u32_dpp v16, v16, v16 quad_perm:[2,3,0,1] row_mask:0xf bank_mask:0xf bound_ctrl:1
	v_add_f32_dpp v17, v17, v17 quad_perm:[2,3,0,1] row_mask:0xf bank_mask:0xf bound_ctrl:1
	v_add_f32_dpp v19, v19, v19 quad_perm:[1,0,3,2] row_mask:0xf bank_mask:0xf bound_ctrl:1
	v_add_u32_dpp v18, v18, v18 quad_perm:[1,0,3,2] row_mask:0xf bank_mask:0xf bound_ctrl:1
	v_add_f32_dpp v17, v17, v17 row_half_mirror row_mask:0xf bank_mask:0xf bound_ctrl:1
	v_add_u32_dpp v16, v16, v16 row_half_mirror row_mask:0xf bank_mask:0xf bound_ctrl:1
	v_add_u32_dpp v18, v18, v18 quad_perm:[2,3,0,1] row_mask:0xf bank_mask:0xf bound_ctrl:1
	v_add_f32_dpp v19, v19, v19 quad_perm:[2,3,0,1] row_mask:0xf bank_mask:0xf bound_ctrl:1
	v_cndmask_b32_e64 v17, v58, v17, s[6:7]
	v_cndmask_b32_e64 v16, v40, v16, s[6:7]
	v_add_f32_dpp v19, v19, v19 row_half_mirror row_mask:0xf bank_mask:0xf bound_ctrl:1
	v_add_u32_dpp v18, v18, v18 row_half_mirror row_mask:0xf bank_mask:0xf bound_ctrl:1
	v_cndmask_b32_e64 v17, v17, v19, s[8:9]
	v_cndmask_b32_e64 v16, v16, v18, s[8:9]
	v_mov_b32_e32 v18, v41
	s_waitcnt vmcnt(3)
	v_cvt_f32_i32_sdwa v19, sext(v20) dst_sel:DWORD dst_unused:UNUSED_PAD src0_sel:BYTE_0
	s_waitcnt vmcnt(2)
	v_dot4c_i32_i8_e32 v18, v20, v24
	v_cvt_f32_i32_sdwa v24, sext(v21) dst_sel:DWORD dst_unused:UNUSED_PAD src0_sel:BYTE_0
	v_dot4c_i32_i8_e32 v18, v21, v25
	v_cvt_f32_i32_sdwa v25, sext(v22) dst_sel:DWORD dst_unused:UNUSED_PAD src0_sel:BYTE_0
	v_dot4c_i32_i8_e32 v18, v22, v26
	v_cvt_f32_i32_sdwa v26, sext(v23) dst_sel:DWORD dst_unused:UNUSED_PAD src0_sel:BYTE_0
	v_fma_f32 v19, v19, v0, 0
	v_fmac_f32_e32 v19, v24, v8
	v_cvt_f32_i32_sdwa v24, sext(v20) dst_sel:DWORD dst_unused:UNUSED_PAD src0_sel:BYTE_1
	v_fmac_f32_e32 v19, v25, v12
	v_cvt_f32_i32_sdwa v25, sext(v21) dst_sel:DWORD dst_unused:UNUSED_PAD src0_sel:BYTE_1
	v_fmac_f32_e32 v19, v26, v4
	v_cvt_f32_i32_sdwa v26, sext(v22) dst_sel:DWORD dst_unused:UNUSED_PAD src0_sel:BYTE_1
	v_cvt_f32_i32_sdwa v32, sext(v23) dst_sel:DWORD dst_unused:UNUSED_PAD src0_sel:BYTE_1
	v_fmac_f32_e32 v19, v24, v1
	v_cvt_f32_i32_sdwa v24, sext(v20) dst_sel:DWORD dst_unused:UNUSED_PAD src0_sel:BYTE_2
	v_fmac_f32_e32 v19, v25, v9
	v_cvt_f32_i32_sdwa v25, sext(v21) dst_sel:DWORD dst_unused:UNUSED_PAD src0_sel:BYTE_2
	v_fmac_f32_e32 v19, v26, v13
	v_cvt_f32_i32_sdwa v26, sext(v22) dst_sel:DWORD dst_unused:UNUSED_PAD src0_sel:BYTE_2
	v_fmac_f32_e32 v19, v32, v5
	v_cvt_f32_i32_sdwa v32, sext(v23) dst_sel:DWORD dst_unused:UNUSED_PAD src0_sel:BYTE_2
	v_fmac_f32_e32 v19, v24, v2
	v_cvt_f32_i32_sdwa v20, sext(v20) dst_sel:DWORD dst_unused:UNUSED_PAD src0_sel:BYTE_3
	v_fmac_f32_e32 v19, v25, v10
	v_cvt_f32_i32_sdwa v21, sext(v21) dst_sel:DWORD dst_unused:UNUSED_PAD src0_sel:BYTE_3
	v_fmac_f32_e32 v19, v26, v14
	v_cvt_f32_i32_sdwa v22, sext(v22) dst_sel:DWORD dst_unused:UNUSED_PAD src0_sel:BYTE_3
	v_fmac_f32_e32 v19, v32, v6
	v_cvt_f32_i32_sdwa v24, sext(v23) dst_sel:DWORD dst_unused:UNUSED_PAD src0_sel:BYTE_3
	v_fmac_f32_e32 v19, v20, v3
	v_fmac_f32_e32 v19, v21, v11
	v_fmac_f32_e32 v19, v22, v15
	v_dot4c_i32_i8_e32 v18, v23, v27
	v_fmac_f32_e32 v19, v24, v7
	s_waitcnt vmcnt(1)
	v_cvt_f32_i32_sdwa v20, sext(v52) dst_sel:DWORD dst_unused:UNUSED_PAD src0_sel:BYTE_0
	v_cvt_f32_i32_sdwa v21, sext(v53) dst_sel:DWORD dst_unused:UNUSED_PAD src0_sel:BYTE_0
	v_add_u32_dpp v18, v18, v18 quad_perm:[1,0,3,2] row_mask:0xf bank_mask:0xf bound_ctrl:1
	v_add_f32_dpp v19, v19, v19 quad_perm:[1,0,3,2] row_mask:0xf bank_mask:0xf bound_ctrl:1
	s_waitcnt vmcnt(0)
	v_dot4c_i32_i8_e32 v41, v50, v54
	v_add_u32_dpp v18, v18, v18 quad_perm:[2,3,0,1] row_mask:0xf bank_mask:0xf bound_ctrl:1
	v_add_f32_dpp v19, v19, v19 quad_perm:[2,3,0,1] row_mask:0xf bank_mask:0xf bound_ctrl:1
	v_dot4c_i32_i8_e32 v41, v51, v55
	v_add_u32_dpp v18, v18, v18 row_half_mirror row_mask:0xf bank_mask:0xf bound_ctrl:1
	v_add_f32_dpp v19, v19, v19 row_half_mirror row_mask:0xf bank_mask:0xf bound_ctrl:1
	v_cndmask_b32_e64 v16, v16, v18, s[10:11]
	v_cvt_f32_i32_sdwa v18, sext(v50) dst_sel:DWORD dst_unused:UNUSED_PAD src0_sel:BYTE_0
	v_cndmask_b32_e64 v17, v17, v19, s[10:11]
	v_cvt_f32_i32_sdwa v19, sext(v51) dst_sel:DWORD dst_unused:UNUSED_PAD src0_sel:BYTE_0
	v_dot4c_i32_i8_e32 v41, v52, v56
	v_fma_f32 v0, v18, v0, 0
	v_cvt_f32_i32_sdwa v18, sext(v53) dst_sel:DWORD dst_unused:UNUSED_PAD src0_sel:BYTE_1
	v_fmac_f32_e32 v0, v19, v8
	v_fmac_f32_e32 v0, v20, v12
	v_fmac_f32_e32 v0, v21, v4
	v_cvt_f32_i32_sdwa v4, sext(v50) dst_sel:DWORD dst_unused:UNUSED_PAD src0_sel:BYTE_1
	v_cvt_f32_i32_sdwa v8, sext(v51) dst_sel:DWORD dst_unused:UNUSED_PAD src0_sel:BYTE_1
	v_cvt_f32_i32_sdwa v12, sext(v52) dst_sel:DWORD dst_unused:UNUSED_PAD src0_sel:BYTE_1
	v_dot4c_i32_i8_e32 v41, v53, v57
	v_fmac_f32_e32 v0, v4, v1
	v_fmac_f32_e32 v0, v8, v9
	v_cvt_f32_i32_sdwa v1, sext(v50) dst_sel:DWORD dst_unused:UNUSED_PAD src0_sel:BYTE_2
	v_fmac_f32_e32 v0, v12, v13
	v_cvt_f32_i32_sdwa v4, sext(v51) dst_sel:DWORD dst_unused:UNUSED_PAD src0_sel:BYTE_2
	v_fmac_f32_e32 v0, v18, v5
	v_cvt_f32_i32_sdwa v5, sext(v52) dst_sel:DWORD dst_unused:UNUSED_PAD src0_sel:BYTE_2
	v_cvt_f32_i32_sdwa v8, sext(v53) dst_sel:DWORD dst_unused:UNUSED_PAD src0_sel:BYTE_2
	v_fmac_f32_e32 v0, v1, v2
	v_cvt_f32_i32_sdwa v1, sext(v50) dst_sel:DWORD dst_unused:UNUSED_PAD src0_sel:BYTE_3
	v_fmac_f32_e32 v0, v4, v10
	v_cvt_f32_i32_sdwa v2, sext(v51) dst_sel:DWORD dst_unused:UNUSED_PAD src0_sel:BYTE_3
	v_fmac_f32_e32 v0, v5, v14
	v_cvt_f32_i32_sdwa v4, sext(v52) dst_sel:DWORD dst_unused:UNUSED_PAD src0_sel:BYTE_3
	v_fmac_f32_e32 v0, v8, v6
	v_cvt_f32_i32_sdwa v5, sext(v53) dst_sel:DWORD dst_unused:UNUSED_PAD src0_sel:BYTE_3
	v_fmac_f32_e32 v0, v1, v3
	v_fmac_f32_e32 v0, v2, v11
	v_fmac_f32_e32 v0, v4, v15
	v_fmac_f32_e32 v0, v5, v7
	v_add_u32_dpp v1, v41, v41 quad_perm:[1,0,3,2] row_mask:0xf bank_mask:0xf bound_ctrl:1
	s_nop 0
	v_add_f32_dpp v0, v0, v0 quad_perm:[1,0,3,2] row_mask:0xf bank_mask:0xf bound_ctrl:1
	v_add_u32_dpp v1, v1, v1 quad_perm:[2,3,0,1] row_mask:0xf bank_mask:0xf bound_ctrl:1
	s_nop 0
	v_add_f32_dpp v0, v0, v0 quad_perm:[2,3,0,1] row_mask:0xf bank_mask:0xf bound_ctrl:1
	v_add_u32_dpp v1, v1, v1 row_half_mirror row_mask:0xf bank_mask:0xf bound_ctrl:1
	v_cndmask_b32_e64 v1, v16, v1, s[12:13]
	v_add_f32_dpp v0, v0, v0 row_half_mirror row_mask:0xf bank_mask:0xf bound_ctrl:1
	v_cndmask_b32_e64 v0, v17, v0, s[12:13]
	global_store_dword v[28:29], v1, off offset:768
	global_store_dword v[30:31], v0, off offset:768
	s_endpgm

	.amdhsa_kernel _Z15k3_pairs_slicedPKDv4_jPKfPKiS5_PiPf
		.amdhsa_group_segment_fixed_size 0
		.amdhsa_private_segment_fixed_size 0
		.amdhsa_kernarg_size 48
		.amdhsa_user_sgpr_count 2
		.amdhsa_user_sgpr_dispatch_ptr 0
		.amdhsa_user_sgpr_queue_ptr 0
		.amdhsa_user_sgpr_kernarg_segment_ptr 1
		.amdhsa_user_sgpr_dispatch_id 0
		.amdhsa_user_sgpr_kernarg_preload_length 0
		.amdhsa_user_sgpr_kernarg_preload_offset 0
		.amdhsa_user_sgpr_private_segment_size 0
		.amdhsa_uses_dynamic_stack 0
		.amdhsa_enable_private_segment 0
		.amdhsa_system_sgpr_workgroup_id_x 1
		.amdhsa_system_sgpr_workgroup_id_y 0
		.amdhsa_system_sgpr_workgroup_id_z 0
		.amdhsa_system_sgpr_workgroup_info 0
		.amdhsa_system_vgpr_workitem_id 0
		.amdhsa_next_free_vgpr 101
		.amdhsa_next_free_sgpr 24
		.amdhsa_accum_offset 104
		.amdhsa_reserve_vcc 1
		.amdhsa_float_round_mode_32 0
		.amdhsa_float_round_mode_16_64 0
		.amdhsa_float_denorm_mode_32 3
		.amdhsa_float_denorm_mode_16_64 3
		.amdhsa_dx10_clamp 1
		.amdhsa_ieee_mode 1
		.amdhsa_fp16_overflow 0
		.amdhsa_tg_split 0
		.amdhsa_exception_fp_ieee_invalid_op 0
		.amdhsa_exception_fp_denorm_src 0
		.amdhsa_exception_fp_ieee_div_zero 0
		.amdhsa_exception_fp_ieee_overflow 0
		.amdhsa_exception_fp_ieee_underflow 0
		.amdhsa_exception_fp_ieee_inexact 0
		.amdhsa_exception_int_div_zero 0
	.end_amdhsa_kernel

_Z10k4_combinePKiPKfS2_S2_Pf:
	s_load_dwordx8 s[16:23], s[0:1], 0x0
	v_lshl_or_b32 v2, s2, 10, v0
	v_lshlrev_b32_e32 v2, 2, v2
	v_add_u32_e32 v3, 0x40000, v2
	v_and_b32_e32 v7, 63, v0
	s_waitcnt lgkmcnt(0)
	s_sub_u32 s12, s16, 0x262a80
	s_subb_u32 s13, s17, 0
	global_load_dword v5, v2, s[20:21]
	global_load_dword v12, v2, s[22:23]
	global_load_dword v18, v3, s[20:21]
	global_load_dword v4, v3, s[22:23]
	v_add_u32_e32 v19, 0x262a80, v2
	global_load_dword v20, v19, s[12:13]
	v_add_u32_e32 v19, 0x262a80, v3
	global_load_dword v28, v19, s[12:13]
	v_add_u32_e32 v19, 0x2e2a80, v2
	global_load_dword v21, v19, s[12:13]
	v_add_u32_e32 v19, 0x2e2a80, v3
	global_load_dword v29, v19, s[12:13]
	v_add_u32_e32 v19, 0x462a80, v2
	global_load_dword v22, v19, s[12:13]
	v_add_u32_e32 v19, 0x462a80, v3
	global_load_dword v30, v19, s[12:13]
	v_add_u32_e32 v19, 0x4e2a80, v2
	global_load_dword v23, v19, s[12:13]
	v_add_u32_e32 v19, 0x4e2a80, v3
	global_load_dword v31, v19, s[12:13]
	v_add_u32_e32 v19, 0x562a80, v2
	global_load_dword v24, v19, s[12:13]
	v_add_u32_e32 v19, 0x562a80, v3
	global_load_dword v32, v19, s[12:13]
	v_add_u32_e32 v19, 0x5e2a80, v2
	global_load_dword v25, v19, s[12:13]
	v_add_u32_e32 v19, 0x5e2a80, v3
	global_load_dword v33, v19, s[12:13]
	v_add_u32_e32 v19, 0x662a80, v2
	global_load_dword v26, v19, s[12:13]
	v_add_u32_e32 v19, 0x662a80, v3
	global_load_dword v34, v19, s[12:13]
	v_add_u32_e32 v19, 0x6e2a80, v2
	global_load_dword v27, v19, s[12:13]
	v_add_u32_e32 v19, 0x6e2a80, v3
	global_load_dword v35, v19, s[12:13]
	v_add_u32_e32 v19, 0x762a80, v2
	global_load_dword v36, v19, s[12:13]
	v_add_u32_e32 v19, 0x762a80, v3
	global_load_dword v44, v19, s[12:13]
	v_add_u32_e32 v19, 0x7e2a80, v2
	global_load_dword v37, v19, s[12:13]
	v_add_u32_e32 v19, 0x7e2a80, v3
	global_load_dword v45, v19, s[12:13]
	v_add_u32_e32 v19, 0x862a80, v2
	global_load_dword v38, v19, s[12:13]
	v_add_u32_e32 v19, 0x862a80, v3
	global_load_dword v46, v19, s[12:13]
	v_add_u32_e32 v19, 0x8e2a80, v2
	global_load_dword v39, v19, s[12:13]
	v_add_u32_e32 v19, 0x8e2a80, v3
	global_load_dword v47, v19, s[12:13]
	v_add_u32_e32 v19, 0x962a80, v2
	global_load_dword v40, v19, s[12:13]
	v_add_u32_e32 v19, 0x962a80, v3
	global_load_dword v48, v19, s[12:13]
	v_add_u32_e32 v19, 0x9e2a80, v2
	global_load_dword v41, v19, s[12:13]
	v_add_u32_e32 v19, 0x9e2a80, v3
	global_load_dword v49, v19, s[12:13]
	v_add_u32_e32 v19, 0x0, v2
	global_load_dword v42, v19, s[12:13]
	v_add_u32_e32 v19, 0x0, v3
	global_load_dword v50, v19, s[12:13]
	v_add_u32_e32 v19, 0x80000, v2
	global_load_dword v43, v19, s[12:13]
	v_add_u32_e32 v19, 0x80000, v3
	global_load_dword v51, v19, s[12:13]
	s_mov_b32 s4, 0xc2ce8ed0
	s_mov_b32 s5, 0x42b17218
	s_mov_b32 s2, 0x3fb8aa3b
	s_mov_b32 s7, 0x800000
	s_mov_b32 s8, 0x3f317217
	s_mov_b32 s6, 0x7f800000
	v_mov_b32_e32 v1, 0
	s_waitcnt vmcnt(0)
	v_mov_b32_e32 v2, v18
	v_mov_b32_e32 v3, 0x7f800000
	v_add_u32_e32 v10, v20, v21
	v_add_u32_e32 v13, v28, v29
	v_add_f32_e32 v11, v36, v37
	v_add_f32_e32 v6, v44, v45
	v_add_u32_e32 v10, v10, v22
	v_add_u32_e32 v13, v13, v30
	v_add_f32_e32 v11, v11, v38
	v_add_f32_e32 v6, v6, v46
	v_add_u32_e32 v10, v10, v23
	v_add_u32_e32 v13, v13, v31
	v_add_f32_e32 v11, v11, v39
	v_add_f32_e32 v6, v6, v47
	v_add_u32_e32 v10, v10, v24
	v_add_u32_e32 v13, v13, v32
	v_add_f32_e32 v11, v11, v40
	v_add_f32_e32 v6, v6, v48
	v_add_u32_e32 v10, v10, v25
	v_add_u32_e32 v13, v13, v33
	v_add_f32_e32 v11, v11, v41
	v_add_f32_e32 v6, v6, v49
	v_add_u32_e32 v10, v10, v26
	v_add_u32_e32 v13, v13, v34
	v_add_f32_e32 v11, v11, v42
	v_add_f32_e32 v6, v6, v50
	v_add_u32_e32 v10, v10, v27
	v_add_u32_e32 v13, v13, v35
	v_add_f32_e32 v11, v11, v43
	v_add_f32_e32 v6, v6, v51
	v_cvt_f32_i32_e32 v8, v10
	s_waitcnt vmcnt(4)
	v_mul_f32_e32 v9, v11, v12
	v_mul_f32_e32 v10, 0x3fb8aa3b, v9
	v_cvt_f32_i32_e32 v11, v13
	v_rndne_f32_e32 v12, v10
	v_cmp_ngt_f32_e32 vcc, s4, v9
	s_waitcnt vmcnt(2)
	v_mul_f32_e32 v4, v6, v4
	v_fma_f32 v6, v9, s2, -v10
	v_mul_f32_e32 v13, 0x3fb8aa3b, v4
	v_fmac_f32_e32 v6, 0x32a5705f, v9
	v_sub_f32_e32 v10, v10, v12
	v_fma_f32 v14, v4, s2, -v13
	v_rndne_f32_e32 v15, v13
	s_waitcnt vmcnt(1)
	v_mul_f32_e32 v5, v5, v8
	v_add_f32_e32 v6, v10, v6
	v_cvt_i32_f32_e32 v12, v12
	v_fmac_f32_e32 v14, 0x32a5705f, v4
	v_sub_f32_e32 v8, v13, v15
	v_mul_f32_e32 v13, 0x3fb8aa3b, v5
	v_exp_f32_e32 v6, v6
	s_waitcnt vmcnt(0)
	v_mul_f32_e32 v2, v2, v11
	v_add_f32_e32 v8, v8, v14
	v_fma_f32 v11, v5, s2, -v13
	v_rndne_f32_e32 v14, v13
	v_cvt_i32_f32_e32 v10, v15
	v_exp_f32_e32 v8, v8
	v_fmac_f32_e32 v11, 0x32a5705f, v5
	v_sub_f32_e32 v13, v13, v14
	v_add_f32_e32 v11, v13, v11
	v_cvt_i32_f32_e32 v14, v14
	v_exp_f32_e32 v11, v11
	v_ldexp_f32 v6, v6, v12
	v_cndmask_b32_e32 v6, 0, v6, vcc
	v_cmp_nlt_f32_e32 vcc, s5, v9
	v_ldexp_f32 v8, v8, v10
	v_mul_f32_e32 v15, 0x3fb8aa3b, v2
	v_cndmask_b32_e32 v6, v3, v6, vcc
	v_cmp_ngt_f32_e32 vcc, s4, v4
	v_fma_f32 v16, v2, s2, -v15
	v_rndne_f32_e32 v17, v15
	v_cndmask_b32_e32 v8, 0, v8, vcc
	v_cmp_nlt_f32_e32 vcc, s5, v4
	v_fmac_f32_e32 v16, 0x32a5705f, v2
	v_sub_f32_e32 v13, v15, v17
	v_cndmask_b32_e32 v4, v3, v8, vcc
	v_ldexp_f32 v8, v11, v14
	v_cmp_ngt_f32_e32 vcc, s4, v5
	v_add_f32_e32 v12, v13, v16
	v_cvt_i32_f32_e32 v15, v17
	v_cndmask_b32_e32 v8, 0, v8, vcc
	v_cmp_nlt_f32_e32 vcc, s5, v5
	v_exp_f32_e32 v12, v12
	s_nop 0
	v_cndmask_b32_e32 v5, v3, v8, vcc
	v_div_scale_f32 v8, s[2:3], v6, v6, v5
	v_rcp_f32_e32 v9, v8
	v_ldexp_f32 v10, v12, v15
	v_div_scale_f32 v11, vcc, v5, v6, v5
	v_fma_f32 v12, -v8, v9, 1.0
	v_fmac_f32_e32 v9, v12, v9
	v_mul_f32_e32 v12, v11, v9
	v_fma_f32 v13, -v8, v12, v11
	v_fmac_f32_e32 v12, v13, v9
	v_fma_f32 v8, -v8, v12, v11
	v_div_fmas_f32 v8, v8, v9, v12
	v_div_fixup_f32 v5, v8, v6, v5
	v_add_f32_e32 v5, 0x322bcc77, v5
	v_cmp_gt_f32_e64 s[2:3], s7, v5
	v_cmp_ngt_f32_e32 vcc, s4, v2
	s_nop 0
	v_cndmask_b32_e64 v6, 0, 32, s[2:3]
	v_ldexp_f32 v5, v5, v6
	v_log_f32_e32 v5, v5
	v_cndmask_b32_e32 v6, 0, v10, vcc
	v_cmp_nlt_f32_e32 vcc, s5, v2
	s_nop 1
	v_cndmask_b32_e32 v2, v3, v6, vcc
	v_div_scale_f32 v6, s[4:5], v4, v4, v2
	v_mul_f32_e32 v3, 0x3f317217, v5
	v_rcp_f32_e32 v8, v6
	v_fma_f32 v3, v5, s8, -v3
	v_fmac_f32_e32 v3, 0x3377d1cf, v5
	v_fmac_f32_e32 v3, 0x3f317217, v5
	v_cmp_lt_f32_e64 vcc, |v5|, s6
	s_nop 1
	v_cndmask_b32_e32 v3, v5, v3, vcc
	v_fma_f32 v5, -v6, v8, 1.0
	v_fmac_f32_e32 v8, v5, v8
	v_div_scale_f32 v5, vcc, v2, v4, v2
	v_mul_f32_e32 v9, v5, v8
	v_fma_f32 v10, -v6, v9, v5
	v_fmac_f32_e32 v9, v10, v8
	v_fma_f32 v5, -v6, v9, v5
	v_div_fmas_f32 v5, v5, v8, v9
	v_div_fixup_f32 v2, v5, v4, v2
	v_add_f32_e32 v2, 0x322bcc77, v2
	v_cmp_gt_f32_e32 vcc, s7, v2
	s_nop 1
	v_cndmask_b32_e64 v4, 0, 32, vcc
	v_ldexp_f32 v2, v2, v4
	v_log_f32_e32 v2, v2
	v_mov_b32_e32 v4, 0x41b17218
	v_cndmask_b32_e64 v5, 0, v4, s[2:3]
	v_sub_f32_e32 v3, v3, v5
	v_mul_f32_e32 v5, 0x3f317217, v2
	v_fma_f32 v5, v2, s8, -v5
	v_fmac_f32_e32 v5, 0x3377d1cf, v2
	v_fmac_f32_e32 v5, 0x3f317217, v2
	v_cmp_lt_f32_e64 s[2:3], |v2|, s6
	v_cndmask_b32_e32 v4, 0, v4, vcc
	v_cmp_eq_u32_e32 vcc, 63, v7
	v_cndmask_b32_e64 v2, v2, v5, s[2:3]
	v_sub_f32_e32 v2, v2, v4
	v_sub_f32_e64 v2, -v2, v3
	v_mov_b32_e32 v3, 0
	s_nop 0
	v_add_f32_dpp v2, v2, v2 quad_perm:[1,0,3,2] row_mask:0xf bank_mask:0xf bound_ctrl:1
	s_nop 1
	v_add_f32_dpp v2, v2, v2 quad_perm:[2,3,0,1] row_mask:0xf bank_mask:0xf bound_ctrl:1
	s_nop 1
	v_add_f32_dpp v2, v2, v2 row_half_mirror row_mask:0xf bank_mask:0xf bound_ctrl:1
	s_nop 1
	v_add_f32_dpp v2, v2, v2 row_mirror row_mask:0xf bank_mask:0xf bound_ctrl:1
	s_nop 1
	v_mov_b32_dpp v3, v2 row_bcast:15 row_mask:0xa bank_mask:0xf
	v_add_f32_e32 v2, v2, v3
	s_nop 1
	v_mov_b32_dpp v1, v2 row_bcast:31 row_mask:0xc bank_mask:0xf
	s_and_saveexec_b64 s[2:3], vcc
	v_lshrrev_b32_e32 v3, 4, v0
	v_and_b32_e32 v3, 60, v3
	v_add_f32_e32 v1, v2, v1
	ds_write_b32 v3, v1
	s_or_b64 exec, exec, s[2:3]
	v_cmp_eq_u32_e32 vcc, 0, v0
	s_waitcnt lgkmcnt(0)
	s_barrier
	s_and_saveexec_b64 s[2:3], vcc
	s_cbranch_execz .LBB3_5
	s_mov_b64 s[2:3], exec
	v_mbcnt_lo_u32_b32 v0, s2, 0
	v_mbcnt_hi_u32_b32 v0, s3, v0
	v_cmp_eq_u32_e32 vcc, 0, v0
	s_and_b64 s[4:5], exec, vcc
	s_mov_b64 exec, s[4:5]
	s_cbranch_execz .LBB3_5
	v_mov_b32_e32 v16, 0
	ds_read_b128 v[0:3], v16
	ds_read_b128 v[4:7], v16 offset:16
	ds_read_b128 v[8:11], v16 offset:32
	ds_read_b128 v[12:15], v16 offset:48
	s_load_dwordx2 s[0:1], s[0:1], 0x20
	s_bcnt1_i32_b64 s2, s[2:3]
	s_waitcnt lgkmcnt(0)
	v_add_f32_e32 v0, 0, v0
	v_add_f32_e32 v0, v0, v1
	v_add_f32_e32 v0, v0, v2
	v_add_f32_e32 v0, v0, v3
	v_add_f32_e32 v0, v0, v4
	v_add_f32_e32 v0, v0, v5
	v_add_f32_e32 v0, v0, v6
	v_add_f32_e32 v0, v0, v7
	v_add_f32_e32 v0, v0, v8
	v_add_f32_e32 v0, v0, v9
	v_add_f32_e32 v0, v0, v10
	v_add_f32_e32 v0, v0, v11
	v_add_f32_e32 v0, v0, v12
	v_add_f32_e32 v0, v0, v13
	v_add_f32_e32 v0, v0, v14
	v_add_f32_e32 v0, v0, v15
	v_mul_f32_e32 v0, 0x37000000, v0
	v_cvt_f32_ubyte0_e32 v1, s2
	v_mul_f32_e32 v0, v0, v1
	global_atomic_add_f32 v16, v0, s[0:1]

	.amdhsa_kernel _Z10k4_combinePKiPKfS2_S2_Pf
		.amdhsa_group_segment_fixed_size 64
		.amdhsa_private_segment_fixed_size 0
		.amdhsa_kernarg_size 40
		.amdhsa_user_sgpr_count 2
		.amdhsa_user_sgpr_dispatch_ptr 0
		.amdhsa_user_sgpr_queue_ptr 0
		.amdhsa_user_sgpr_kernarg_segment_ptr 1
		.amdhsa_user_sgpr_dispatch_id 0
		.amdhsa_user_sgpr_kernarg_preload_length 0
		.amdhsa_user_sgpr_kernarg_preload_offset 0
		.amdhsa_user_sgpr_private_segment_size 0
		.amdhsa_uses_dynamic_stack 0
		.amdhsa_enable_private_segment 0
		.amdhsa_system_sgpr_workgroup_id_x 1
		.amdhsa_system_sgpr_workgroup_id_y 0
		.amdhsa_system_sgpr_workgroup_id_z 0
		.amdhsa_system_sgpr_workgroup_info 0
		.amdhsa_system_vgpr_workitem_id 0
		.amdhsa_next_free_vgpr 52
		.amdhsa_next_free_sgpr 24
		.amdhsa_accum_offset 52
		.amdhsa_reserve_vcc 1
		.amdhsa_float_round_mode_32 0
		.amdhsa_float_round_mode_16_64 0
		.amdhsa_float_denorm_mode_32 3
		.amdhsa_float_denorm_mode_16_64 3
		.amdhsa_dx10_clamp 1
		.amdhsa_ieee_mode 1
		.amdhsa_fp16_overflow 0
		.amdhsa_tg_split 0
		.amdhsa_exception_fp_ieee_invalid_op 0
		.amdhsa_exception_fp_denorm_src 0
		.amdhsa_exception_fp_ieee_div_zero 0
		.amdhsa_exception_fp_ieee_overflow 0
		.amdhsa_exception_fp_ieee_underflow 0
		.amdhsa_exception_fp_ieee_inexact 0
		.amdhsa_exception_int_div_zero 0
	.end_amdhsa_kernel
